# mLSTM pass-2 h stores widened: v_permlane32_swap pairs then 2 x dwordx4 per row instead of 4 x dwordx2
# speedup vs baseline: 1.0123x; 1.0123x over previous
; #define LAS __attribute__((address_space(3)))
; template <bool PASS2, int DIRT>
; DI void mlstm_item(const Params& P, LAS unsigned char* lds, int st, int g) {
;     ...
;             { const int j = tid & 127, part = tid >> 7; float s = 0.f;
; #pragma unroll
;               for (int cc = 0; cc < 4; ++cc) { const u32x4 q8 = *(const LAS u32x4*)(QS + off_b(j, 4 * part + cc)); const f32x4 n0a = *(const LAS f32x4*)(sN0 + 32 * part + 8 * cc), n0b = *(const LAS f32x4*)(sN0 + 32 * part + 8 * cc + 4);
;                   s += bf_lo(q8.x) * n0a[0] + bf_hi(q8.x) * n0a[1] + bf_lo(q8.y) * n0a[2] + bf_hi(q8.y) * n0a[3] + bf_lo(q8.z) * n0b[0] + bf_hi(q8.z) * n0b[1] + bf_lo(q8.w) * n0b[2] + bf_hi(q8.w) * n0b[3]; }
;               sQNP[part * 128 + j] = s; }
;             tid = (wid << 6) | lane_id(); asm volatile("" : "+v"(tid)); lane = tid & 63; r = lane & 31; hh = lane >> 5;
; #pragma unroll
;             for (int jt = 0; jt < 4; ++jt)
; #pragma unroll
;                 for (int e = 0; e < 16; ++e) num[jt][e] = 0.f;
;             {
;                 bf16x8 qf[2][4];
;                 auto ldq = [&](int g_, bf16x8 (&qb)[4]) { const int dkt = g_ >> 1, s2 = g_ & 1;
; #pragma unroll
;                     for (int jt = 0; jt < 4; ++jt) { const s16x4 lo = *(const LAS s16x4*)(QS + off_b(32 * jt + r, 4 * dkt + 2 * s2) + 8 * hh); const s16x4 hi = *(const LAS s16x4*)(QS + off_b(32 * jt + r, 4 * dkt + 2 * s2 + 1) + 8 * hh);
;                         qb[jt] = __builtin_shufflevector(lo, hi, 0, 1, 2, 3, 4, 5, 6, 7); } };
;                 ldq(0, qf[0]);
; #pragma unroll
;                 for (int g_ = 0; g_ < 8; ++g_) { const int dkt = g_ >> 1, s2 = g_ & 1;
;                     if (g_ + 1 < 8) ldq(g_ + 1, qf[(g_ + 1) & 1]);
;                     __builtin_amdgcn_sched_barrier(0);
;                     u32x4 xp; xp.x = pk2(C[dkt][8 * s2 + 0], C[dkt][8 * s2 + 1]); xp.y = pk2(C[dkt][8 * s2 + 2], C[dkt][8 * s2 + 3]); xp.z = pk2(C[dkt][8 * s2 + 4], C[dkt][8 * s2 + 5]); xp.w = pk2(C[dkt][8 * s2 + 6], C[dkt][8 * s2 + 7]);
;                     const bf16x8 xs = __builtin_bit_cast(bf16x8, xp);
; #pragma unroll
;                     for (int jt = 0; jt < 4; ++jt) num[jt] = MFMA32(xs, qf[g_ & 1][jt], num[jt]);
;                     __builtin_amdgcn_sched_barrier(0);
;                     if (s2 == 1) asm volatile("" : "+v"(num[0]), "+v"(num[1]), "+v"(num[2]), "+v"(num[3]) :: "memory"); }
.LBB0_755:
	s_and_saveexec_b64 s[2:3], s[44:45]
	ds_write_b32 v86, v64 offset:128
	s_or_b64 exec, exec, s[2:3]
	v_and_b32_e32 v65, 0xffffff80, v80
	v_add_u32_e32 v65, 0, v65
	v_and_b32_e32 v64, 0x7f, v80
	v_add_u32_e32 v81, 0x1a600, v65
	v_ashrrev_i32_e32 v65, 1, v80
	v_mul_u32_u24_e32 v64, 0x110, v64
	v_and_b32_e32 v65, 0xffffffc0, v65
	v_add3_u32 v76, 0, v64, v65
	s_waitcnt lgkmcnt(1)
	ds_read_b128 v[64:67], v76
	ds_read_b128 v[68:71], v76 offset:16
	ds_read_b128 v[72:75], v76 offset:32
	ds_read_b128 v[76:79], v76 offset:48
	ds_read_b128 v[82:85], v81
	ds_read_b128 v[86:89], v81 offset:16
	ds_read_b128 v[90:93], v81 offset:32
	ds_read_b128 v[94:97], v81 offset:48
	s_waitcnt lgkmcnt(6)
	v_and_b32_e32 v103, 0xffff0000, v68
	v_and_b32_e32 v102, 0xffff0000, v64
	v_lshlrev_b32_e32 v99, 16, v68
	s_waitcnt lgkmcnt(1)
	v_mov_b32_e32 v101, v90
	v_mov_b32_e32 v90, v83
	v_lshlrev_b32_e32 v98, 16, v64
	v_mov_b32_e32 v100, v82
	v_pk_mul_f32 v[82:83], v[90:91], v[102:103]
	v_lshlrev_b32_e32 v91, 16, v69
	v_pk_fma_f32 v[82:83], v[100:101], v[98:99], v[82:83]
	v_lshlrev_b32_e32 v90, 16, v65
	v_mov_b32_e32 v98, v84
	v_mov_b32_e32 v99, v92
	v_pk_fma_f32 v[82:83], v[98:99], v[90:91], v[82:83]
	v_and_b32_e32 v69, 0xffff0000, v69
	v_and_b32_e32 v68, 0xffff0000, v65
	v_mov_b32_e32 v92, v85
	v_pk_fma_f32 v[64:65], v[92:93], v[68:69], v[82:83]
	v_lshlrev_b32_e32 v69, 16, v70
	v_lshlrev_b32_e32 v68, 16, v66
	v_mov_b32_e32 v82, v86
	s_waitcnt lgkmcnt(0)
	v_mov_b32_e32 v83, v94
	v_pk_fma_f32 v[64:65], v[82:83], v[68:69], v[64:65]
	v_and_b32_e32 v69, 0xffff0000, v70
	v_and_b32_e32 v68, 0xffff0000, v66
	v_mov_b32_e32 v94, v87
	v_pk_fma_f32 v[64:65], v[94:95], v[68:69], v[64:65]
	v_lshlrev_b32_e32 v69, 16, v71
	v_lshlrev_b32_e32 v68, 16, v67
	v_mov_b32_e32 v82, v88
	v_mov_b32_e32 v83, v96
	v_pk_fma_f32 v[64:65], v[82:83], v[68:69], v[64:65]
	v_and_b32_e32 v69, 0xffff0000, v71
	v_and_b32_e32 v68, 0xffff0000, v67
	v_mov_b32_e32 v96, v89
	v_pk_fma_f32 v[64:65], v[96:97], v[68:69], v[64:65]
	v_and_b32_e32 v95, 0xffff0000, v76
	v_add_f32_e32 v64, 0, v64
	v_add_f32_e32 v96, v64, v65
	ds_read_b128 v[64:67], v81 offset:64
	ds_read_b128 v[68:71], v81 offset:80
	ds_read_b128 v[82:85], v81 offset:96
	ds_read_b128 v[86:89], v81 offset:112
	v_and_b32_e32 v94, 0xffff0000, v72
	v_lshlrev_b32_e32 v91, 16, v76
	v_lshlrev_b32_e32 v90, 16, v72
	s_waitcnt lgkmcnt(1)
	v_mov_b32_e32 v93, v82
	v_mov_b32_e32 v82, v65
	v_mov_b32_e32 v92, v64
	v_pk_mul_f32 v[64:65], v[82:83], v[94:95]
	v_lshlrev_b32_e32 v83, 16, v77
	v_pk_fma_f32 v[64:65], v[92:93], v[90:91], v[64:65]
	v_lshlrev_b32_e32 v82, 16, v73
	v_mov_b32_e32 v90, v66
	v_mov_b32_e32 v91, v84
	v_pk_fma_f32 v[64:65], v[90:91], v[82:83], v[64:65]
	v_and_b32_e32 v77, 0xffff0000, v77
	v_and_b32_e32 v76, 0xffff0000, v73
	v_mov_b32_e32 v84, v67
	v_pk_fma_f32 v[64:65], v[84:85], v[76:77], v[64:65]
	v_lshlrev_b32_e32 v67, 16, v78
	v_lshlrev_b32_e32 v66, 16, v74
	v_mov_b32_e32 v72, v68
	s_waitcnt lgkmcnt(0)
	v_mov_b32_e32 v73, v86
	v_pk_fma_f32 v[64:65], v[72:73], v[66:67], v[64:65]
	v_and_b32_e32 v67, 0xffff0000, v78
	v_and_b32_e32 v66, 0xffff0000, v74
	v_mov_b32_e32 v86, v69
	v_pk_fma_f32 v[64:65], v[86:87], v[66:67], v[64:65]
	v_lshlrev_b32_e32 v67, 16, v79
	v_lshlrev_b32_e32 v66, 16, v75
	v_mov_b32_e32 v68, v70
	v_mov_b32_e32 v69, v88
	v_pk_fma_f32 v[64:65], v[68:69], v[66:67], v[64:65]
	v_and_b32_e32 v67, 0xffff0000, v79
	v_and_b32_e32 v66, 0xffff0000, v75
	v_mov_b32_e32 v88, v71
	v_pk_fma_f32 v[64:65], v[88:89], v[66:67], v[64:65]
	s_nop 0
	v_add_f32_e32 v64, v96, v64
	v_add_f32_e32 v64, v64, v65
	v_lshl_add_u32 v65, v80, 2, s95
	ds_write_b32 v65, v64
	v_mbcnt_lo_u32_b32 v64, -1, 0
	v_mbcnt_hi_u32_b32 v64, -1, v64
	s_nop 0
	v_or_b32_e32 v64, s97, v64
	s_nop 0
	v_and_b32_e32 v192, 31, v64
	v_lshrrev_b32_e32 v64, 2, v64
	v_mul_u32_u24_e32 v65, 0x110, v192
	v_and_b32_e32 v64, 8, v64
	v_add3_u32 v196, 0, v65, v64
	v_add_u32_e32 v197, 0x2000, v196
	v_add_u32_e32 v242, 0x4000, v196
	v_add_u32_e32 v243, 0x6000, v196
	ds_read2_b64 v[64:67], v196 offset1:2
	ds_read2_b64 v[206:209], v196 offset0:4 offset1:6
	ds_read2_b64 v[68:71], v197 offset0:64 offset1:66
	ds_read2_b64 v[72:75], v242 offset0:128 offset1:130
	ds_read2_b64 v[76:79], v243 offset0:192 offset1:194
	ds_read2_b64 v[210:213], v197 offset0:68 offset1:70
	ds_read2_b64 v[214:217], v242 offset0:132 offset1:134
	ds_read2_b64 v[218:221], v243 offset0:196 offset1:198
	v_cvt_pk_bf16_f32 v222, v0, v1
	v_cvt_pk_bf16_f32 v223, v2, v3
	v_cvt_pk_bf16_f32 v224, v4, v5
	v_cvt_pk_bf16_f32 v225, v6, v7
	s_waitcnt lgkmcnt(7)
	s_nop 0
	v_mfma_f32_32x32x16_bf16 v[112:127], v[222:225], v[64:67], 0
	s_waitcnt lgkmcnt(5)
	v_mfma_f32_32x32x16_bf16 v[96:111], v[222:225], v[68:71], 0
	s_waitcnt lgkmcnt(4)
	v_mfma_f32_32x32x16_bf16 v[80:95], v[222:225], v[72:75], 0
	s_waitcnt lgkmcnt(3)
	v_mfma_f32_32x32x16_bf16 v[64:79], v[222:225], v[76:79], 0
	ds_read2_b64 v[222:225], v196 offset0:8 offset1:10
	ds_read2_b64 v[226:229], v197 offset0:72 offset1:74
	ds_read2_b64 v[230:233], v242 offset0:136 offset1:138
	ds_read2_b64 v[234:237], v243 offset0:200 offset1:202
	v_cvt_pk_bf16_f32 v238, v8, v9
	v_cvt_pk_bf16_f32 v239, v10, v11
	v_cvt_pk_bf16_f32 v240, v12, v13
	v_cvt_pk_bf16_f32 v241, v14, v15
	s_waitcnt lgkmcnt(6)
	s_nop 0
	v_mfma_f32_32x32x16_bf16 v[96:111], v[238:241], v[210:213], v[96:111]
	s_waitcnt lgkmcnt(5)
	v_mfma_f32_32x32x16_bf16 v[80:95], v[238:241], v[214:217], v[80:95]
	s_waitcnt lgkmcnt(4)
; DI unsigned pk2(float a, float b) { f32x2 f = {a, b}; bf16x2_t h = __builtin_convertvector(f, bf16x2_t); return __builtin_bit_cast(unsigned, h); }
; #define MFMA32(a, b, c) __builtin_amdgcn_mfma_f32_32x32x16_bf16((a), (b), (c), 0, 0, 0)
; template <bool PASS2, int DIRT>
; DI void mlstm_item(const Params& P, LAS unsigned char* lds, int st, int g) {
;     ...
;                 for (int g_ = 0; g_ < 8; ++g_) { const int dkt = g_ >> 1, s2 = g_ & 1;
;                     if (g_ + 1 < 8) ldq(g_ + 1, qf[(g_ + 1) & 1]);
;                     __builtin_amdgcn_sched_barrier(0);
;                     u32x4 xp; xp.x = pk2(C[dkt][8 * s2 + 0], C[dkt][8 * s2 + 1]); xp.y = pk2(C[dkt][8 * s2 + 2], C[dkt][8 * s2 + 3]); xp.z = pk2(C[dkt][8 * s2 + 4], C[dkt][8 * s2 + 5]); xp.w = pk2(C[dkt][8 * s2 + 6], C[dkt][8 * s2 + 7]);
;                     const bf16x8 xs = __builtin_bit_cast(bf16x8, xp);
; #pragma unroll
;                     for (int jt = 0; jt < 4; ++jt) num[jt] = MFMA32(xs, qf[g_ & 1][jt], num[jt]);
;                     __builtin_amdgcn_sched_barrier(0);
;                     if (s2 == 1) asm volatile("" : "+v"(num[0]), "+v"(num[1]), "+v"(num[2]), "+v"(num[3]) :: "memory"); }
;             }
; #pragma unroll
;             for (int jt = 0; jt < 4; ++jt) { const float ws_ = sWST[32 * jt + r];
; #pragma unroll
;                 for (int e = 0; e < 16; ++e) num[jt][e] *= ws_; }
;             __syncthreads();
	v_mfma_f32_32x32x16_bf16 v[64:79], v[238:241], v[218:221], v[64:79]
	v_mfma_f32_32x32x16_bf16 v[112:127], v[238:241], v[206:209], v[112:127]
	ds_read2_b64 v[206:209], v196 offset0:12 offset1:14
	ds_read2_b64 v[210:213], v197 offset0:76 offset1:78
	ds_read2_b64 v[214:217], v242 offset0:140 offset1:142
	ds_read2_b64 v[218:221], v243 offset0:204 offset1:206
	v_cvt_pk_bf16_f32 v238, v16, v17
	v_cvt_pk_bf16_f32 v239, v18, v19
	v_cvt_pk_bf16_f32 v240, v20, v21
	v_cvt_pk_bf16_f32 v241, v22, v23
	s_waitcnt lgkmcnt(6)
	s_nop 0
	v_mfma_f32_32x32x16_bf16 v[96:111], v[238:241], v[226:229], v[96:111]
	s_waitcnt lgkmcnt(5)
	v_mfma_f32_32x32x16_bf16 v[80:95], v[238:241], v[230:233], v[80:95]
	s_waitcnt lgkmcnt(4)
	v_mfma_f32_32x32x16_bf16 v[64:79], v[238:241], v[234:237], v[64:79]
	v_mfma_f32_32x32x16_bf16 v[112:127], v[238:241], v[222:225], v[112:127]
	ds_read2_b64 v[222:225], v196 offset0:16 offset1:18
	ds_read2_b64 v[226:229], v197 offset0:80 offset1:82
	ds_read2_b64 v[230:233], v242 offset0:144 offset1:146
	ds_read2_b64 v[234:237], v243 offset0:208 offset1:210
	v_cvt_pk_bf16_f32 v238, v24, v25
	v_cvt_pk_bf16_f32 v239, v26, v27
	v_cvt_pk_bf16_f32 v240, v28, v29
	v_cvt_pk_bf16_f32 v241, v30, v31
	s_waitcnt lgkmcnt(6)
	s_nop 0
	v_mfma_f32_32x32x16_bf16 v[96:111], v[238:241], v[210:213], v[96:111]
	s_waitcnt lgkmcnt(5)
	v_mfma_f32_32x32x16_bf16 v[80:95], v[238:241], v[214:217], v[80:95]
	s_waitcnt lgkmcnt(4)
	v_mfma_f32_32x32x16_bf16 v[64:79], v[238:241], v[218:221], v[64:79]
	v_mfma_f32_32x32x16_bf16 v[112:127], v[238:241], v[206:209], v[112:127]
	ds_read2_b64 v[206:209], v196 offset0:20 offset1:22
	ds_read2_b64 v[210:213], v197 offset0:84 offset1:86
	ds_read2_b64 v[214:217], v242 offset0:148 offset1:150
	ds_read2_b64 v[218:221], v243 offset0:212 offset1:214
	v_cvt_pk_bf16_f32 v238, v32, v33
	v_cvt_pk_bf16_f32 v239, v34, v35
	v_cvt_pk_bf16_f32 v240, v36, v37
	v_cvt_pk_bf16_f32 v241, v38, v39
	s_waitcnt lgkmcnt(6)
	s_nop 0
	v_mfma_f32_32x32x16_bf16 v[96:111], v[238:241], v[226:229], v[96:111]
	s_waitcnt lgkmcnt(5)
	v_mfma_f32_32x32x16_bf16 v[80:95], v[238:241], v[230:233], v[80:95]
	s_waitcnt lgkmcnt(4)
	v_mfma_f32_32x32x16_bf16 v[64:79], v[238:241], v[234:237], v[64:79]
	v_mfma_f32_32x32x16_bf16 v[112:127], v[238:241], v[222:225], v[112:127]
	ds_read2_b64 v[222:225], v196 offset0:24 offset1:26
	ds_read2_b64 v[226:229], v197 offset0:88 offset1:90
	ds_read2_b64 v[230:233], v242 offset0:152 offset1:154
	ds_read2_b64 v[234:237], v243 offset0:216 offset1:218
	v_cvt_pk_bf16_f32 v238, v40, v41
	v_cvt_pk_bf16_f32 v239, v42, v43
	v_cvt_pk_bf16_f32 v240, v44, v45
	v_cvt_pk_bf16_f32 v241, v46, v47
	s_waitcnt lgkmcnt(6)
	s_nop 0
	v_mfma_f32_32x32x16_bf16 v[96:111], v[238:241], v[210:213], v[96:111]
	s_waitcnt lgkmcnt(5)
	v_mfma_f32_32x32x16_bf16 v[80:95], v[238:241], v[214:217], v[80:95]
	s_waitcnt lgkmcnt(4)
	v_mfma_f32_32x32x16_bf16 v[64:79], v[238:241], v[218:221], v[64:79]
	v_mfma_f32_32x32x16_bf16 v[112:127], v[238:241], v[206:209], v[112:127]
	ds_read2_b64 v[206:209], v196 offset0:28 offset1:30
	ds_read2_b64 v[210:213], v197 offset0:92 offset1:94
	ds_read2_b64 v[214:217], v242 offset0:156 offset1:158
	ds_read2_b64 v[218:221], v243 offset0:220 offset1:222
	v_cvt_pk_bf16_f32 v238, v48, v49
	v_cvt_pk_bf16_f32 v239, v50, v51
	v_cvt_pk_bf16_f32 v240, v52, v53
	v_cvt_pk_bf16_f32 v241, v54, v55
	s_waitcnt lgkmcnt(6)
	s_nop 0
	v_mfma_f32_32x32x16_bf16 v[96:111], v[238:241], v[226:229], v[96:111]
	s_waitcnt lgkmcnt(5)
	v_mfma_f32_32x32x16_bf16 v[80:95], v[238:241], v[230:233], v[80:95]
	s_waitcnt lgkmcnt(4)
	v_mfma_f32_32x32x16_bf16 v[64:79], v[238:241], v[234:237], v[64:79]
	v_mfma_f32_32x32x16_bf16 v[112:127], v[238:241], v[222:225], v[112:127]
	v_cvt_pk_bf16_f32 v222, v56, v57
	v_cvt_pk_bf16_f32 v223, v58, v59
	v_cvt_pk_bf16_f32 v224, v60, v61
	v_cvt_pk_bf16_f32 v225, v62, v63
	s_waitcnt lgkmcnt(2)
	s_nop 0
	v_mfma_f32_32x32x16_bf16 v[96:111], v[222:225], v[210:213], v[96:111]
	s_waitcnt lgkmcnt(1)
	v_mfma_f32_32x32x16_bf16 v[80:95], v[222:225], v[214:217], v[80:95]
	s_waitcnt lgkmcnt(0)
	v_mfma_f32_32x32x16_bf16 v[64:79], v[222:225], v[218:221], v[64:79]
	v_mfma_f32_32x32x16_bf16 v[112:127], v[222:225], v[206:209], v[112:127]
	s_add_i32 s2, 0, 0x19c00
	v_lshl_add_u32 v206, v192, 2, s2
	ds_read2_b32 v[196:197], v206 offset1:32
	s_add_i32 s3, 0, 0x11000
	s_waitcnt lgkmcnt(0)
	s_nop 6
	v_pk_mul_f32 v[126:127], v[196:197], v[126:127] op_sel_hi:[0,1]
	v_pk_mul_f32 v[124:125], v[196:197], v[124:125] op_sel_hi:[0,1]
	v_pk_mul_f32 v[122:123], v[196:197], v[122:123] op_sel_hi:[0,1]
	v_pk_mul_f32 v[120:121], v[196:197], v[120:121] op_sel_hi:[0,1]
	v_pk_mul_f32 v[118:119], v[196:197], v[118:119] op_sel_hi:[0,1]
	v_pk_mul_f32 v[116:117], v[196:197], v[116:117] op_sel_hi:[0,1]
	v_pk_mul_f32 v[114:115], v[196:197], v[114:115] op_sel_hi:[0,1]
	v_pk_mul_f32 v[112:113], v[196:197], v[112:113] op_sel_hi:[0,1]
	v_mov_b32_e32 v192, v197
	ds_read2_b32 v[196:197], v206 offset0:64 offset1:96
	v_pk_mul_f32 v[110:111], v[192:193], v[110:111] op_sel_hi:[0,1]
	v_pk_mul_f32 v[108:109], v[192:193], v[108:109] op_sel_hi:[0,1]
	v_pk_mul_f32 v[106:107], v[192:193], v[106:107] op_sel_hi:[0,1]
	v_pk_mul_f32 v[104:105], v[192:193], v[104:105] op_sel_hi:[0,1]
	v_pk_mul_f32 v[102:103], v[192:193], v[102:103] op_sel_hi:[0,1]
	v_pk_mul_f32 v[100:101], v[192:193], v[100:101] op_sel_hi:[0,1]
	v_pk_mul_f32 v[98:99], v[192:193], v[98:99] op_sel_hi:[0,1]
	v_pk_mul_f32 v[96:97], v[192:193], v[96:97] op_sel_hi:[0,1]
	s_waitcnt lgkmcnt(0)
	v_mov_b32_e32 v192, v197
	v_pk_mul_f32 v[78:79], v[78:79], v[192:193] op_sel_hi:[1,0]
	v_pk_mul_f32 v[76:77], v[76:77], v[192:193] op_sel_hi:[1,0]
	v_pk_mul_f32 v[74:75], v[74:75], v[192:193] op_sel_hi:[1,0]
	v_pk_mul_f32 v[72:73], v[72:73], v[192:193] op_sel_hi:[1,0]
	v_pk_mul_f32 v[70:71], v[70:71], v[192:193] op_sel_hi:[1,0]
	v_pk_mul_f32 v[68:69], v[68:69], v[192:193] op_sel_hi:[1,0]
	v_pk_mul_f32 v[66:67], v[66:67], v[192:193] op_sel_hi:[1,0]
	v_pk_mul_f32 v[64:65], v[64:65], v[192:193] op_sel_hi:[1,0]
	s_barrier
; #define LAS __attribute__((address_space(3)))
; DI unsigned pk2(float a, float b) { f32x2 f = {a, b}; bf16x2_t h = __builtin_convertvector(f, bf16x2_t); return __builtin_bit_cast(unsigned, h); }
; #define MFMA32(a, b, c) __builtin_amdgcn_mfma_f32_32x32x16_bf16((a), (b), (c), 0, 0, 0)
; template <bool PASS2, int DIRT>
; DI void mlstm_item(const Params& P, LAS unsigned char* lds, int st, int g) {
;     ...
;             {
;                 bf16x8 pf[2][4];
;                 auto ldp = [&](int ks, bf16x8 (&pb)[4]) {
; #pragma unroll
;                     for (int jt = 0; jt < 4; ++jt) { const bool on = dir ? (ks >= 2 * jt) : (ks <= 2 * jt + 1); if (on) pb[jt] = *(const LAS bf16x8*)(PS + off_b(32 * jt + r, 2 * ks + hh)); } };
;                 ldp(0, pf[0]);
; #pragma unroll
;                 for (int ks = 0; ks < 8; ++ks) {
;                     if (ks + 1 < 8) ldp(ks + 1, pf[(ks + 1) & 1]);
;                     __builtin_amdgcn_sched_barrier(0);
; #pragma unroll
;                     for (int jt = 0; jt < 4; ++jt) { const bool on = dir ? (ks >= 2 * jt) : (ks <= 2 * jt + 1); if (on) num[jt] = MFMA32(vf[ks], pf[ks & 1][jt], num[jt]); }
;                     __builtin_amdgcn_sched_barrier(0); }
;                 asm volatile("" : "+v"(num[0]), "+v"(num[1]), "+v"(num[2]), "+v"(num[3]) :: "memory");
;             }
;             bf16_t* Hd = (bf16_t*)(P.ws + (dir ? WS_HB : WS_HF));
; #pragma unroll
;             for (int jt = 0; jt < 4; ++jt) { const int j = 32 * jt + r;
;                 const float den = (sDENP[j] + sDENP[128 + j]) + (sDENP[256 + j] + sDENP[384 + j]) + sWST[j] * ((sQNP[j] + sQNP[128 + j]) + (sQNP[256 + j] + sQNP[384 + j]));
;                 const float inv = 1.0f / fmaxf(fabsf(den), sCL[j]);
;                 bf16_t* hp = Hd + (size_t)(tok0 + j) * 1024 + h * 256 + 32 * wid + 4 * hh;
; #pragma unroll
;                 for (int gq = 0; gq < 4; ++gq) { u32x2 w; w.x = pk2(num[jt][4 * gq] * inv, num[jt][4 * gq + 1] * inv); w.y = pk2(num[jt][4 * gq + 2] * inv, num[jt][4 * gq + 3] * inv); *(u32x2*)(hp + 8 * gq) = w; } }
	v_mbcnt_lo_u32_b32 v192, -1, 0
	v_mbcnt_hi_u32_b32 v192, -1, v192
	v_pk_mul_f32 v[94:95], v[94:95], v[196:197] op_sel_hi:[1,0]
	v_or_b32_e32 v192, s97, v192
	v_pk_mul_f32 v[92:93], v[92:93], v[196:197] op_sel_hi:[1,0]
	v_and_b32_e32 v206, 31, v192
	v_bfe_u32 v192, v192, 5, 1
	v_pk_mul_f32 v[90:91], v[90:91], v[196:197] op_sel_hi:[1,0]
	v_pk_mul_f32 v[88:89], v[88:89], v[196:197] op_sel_hi:[1,0]
	v_pk_mul_f32 v[86:87], v[86:87], v[196:197] op_sel_hi:[1,0]
	v_pk_mul_f32 v[84:85], v[84:85], v[196:197] op_sel_hi:[1,0]
	v_pk_mul_f32 v[82:83], v[82:83], v[196:197] op_sel_hi:[1,0]
	v_pk_mul_f32 v[80:81], v[80:81], v[196:197] op_sel_hi:[1,0]
	v_mul_u32_u24_e32 v196, 0x110, v206
	v_lshlrev_b32_e32 v197, 4, v192
	v_add3_u32 v196, s3, v197, v196
	ds_read_b128 v[208:211], v196
	ds_read_b128 v[212:215], v196 offset:32
	s_waitcnt vmcnt(7) lgkmcnt(1)
	v_mfma_f32_32x32x16_bf16 v[112:127], v[188:191], v[208:211], v[112:127]
	ds_read_b128 v[208:211], v196 offset:64
	ds_read_b128 v[216:219], v196 offset:8768
	s_waitcnt vmcnt(6) lgkmcnt(2)
	v_mfma_f32_32x32x16_bf16 v[112:127], v[184:187], v[212:215], v[112:127]
	ds_read_b128 v[212:215], v196 offset:96
	ds_read_b128 v[220:223], v196 offset:8800
	s_waitcnt vmcnt(5) lgkmcnt(2)
	v_mfma_f32_32x32x16_bf16 v[96:111], v[180:183], v[216:219], v[96:111]
	v_mfma_f32_32x32x16_bf16 v[112:127], v[180:183], v[208:211], v[112:127]
	ds_read_b128 v[208:211], v196 offset:128
	ds_read_b128 v[216:219], v196 offset:8832
	ds_read_b128 v[224:227], v196 offset:17536
	s_waitcnt vmcnt(4) lgkmcnt(3)
	v_mfma_f32_32x32x16_bf16 v[96:111], v[176:179], v[220:223], v[96:111]
	v_mfma_f32_32x32x16_bf16 v[112:127], v[176:179], v[212:215], v[112:127]
	ds_read_b128 v[212:215], v196 offset:160
	ds_read_b128 v[220:223], v196 offset:8864
	ds_read_b128 v[228:231], v196 offset:17568
	s_waitcnt vmcnt(3) lgkmcnt(4)
	v_mfma_f32_32x32x16_bf16 v[96:111], v[172:175], v[216:219], v[96:111]
	s_waitcnt lgkmcnt(3)
	v_mfma_f32_32x32x16_bf16 v[80:95], v[172:175], v[224:227], v[80:95]
	v_mfma_f32_32x32x16_bf16 v[112:127], v[172:175], v[208:211], v[112:127]
	ds_read_b128 v[208:211], v196 offset:192
	ds_read_b128 v[216:219], v196 offset:8896
	ds_read_b128 v[224:227], v196 offset:17600
	ds_read_b128 v[232:235], v196 offset:26304
	s_waitcnt vmcnt(2) lgkmcnt(5)
	v_mfma_f32_32x32x16_bf16 v[96:111], v[168:171], v[220:223], v[96:111]
	s_waitcnt lgkmcnt(4)
	v_mfma_f32_32x32x16_bf16 v[80:95], v[168:171], v[228:231], v[80:95]
	v_mfma_f32_32x32x16_bf16 v[112:127], v[168:171], v[212:215], v[112:127]
	ds_read_b128 v[212:215], v196 offset:224
	ds_read_b128 v[220:223], v196 offset:8928
	ds_read_b128 v[228:231], v196 offset:17632
	ds_read_b128 v[236:239], v196 offset:26336
	s_waitcnt vmcnt(1) lgkmcnt(6)
	v_mfma_f32_32x32x16_bf16 v[96:111], v[164:167], v[216:219], v[96:111]
	s_waitcnt lgkmcnt(5)
	v_mfma_f32_32x32x16_bf16 v[80:95], v[164:167], v[224:227], v[80:95]
	s_waitcnt lgkmcnt(4)
	v_mfma_f32_32x32x16_bf16 v[64:79], v[164:167], v[232:235], v[64:79]
	v_mfma_f32_32x32x16_bf16 v[112:127], v[164:167], v[208:211], v[112:127]
	s_waitcnt vmcnt(0) lgkmcnt(2)
	v_mfma_f32_32x32x16_bf16 v[96:111], v[160:163], v[220:223], v[96:111]
	s_waitcnt lgkmcnt(1)
	v_mfma_f32_32x32x16_bf16 v[80:95], v[160:163], v[228:231], v[80:95]
	s_waitcnt lgkmcnt(0)
	v_mfma_f32_32x32x16_bf16 v[64:79], v[160:163], v[236:239], v[64:79]
	v_mfma_f32_32x32x16_bf16 v[112:127], v[160:163], v[212:215], v[112:127]
	v_lshlrev_b32_e32 v192, 3, v192
	s_add_i32 s3, 0, 0x1a800
	v_lshlrev_b32_e32 v207, 2, v206
	v_lshl_add_u64 v[196:197], s[14:15], 0, v[192:193]
	v_add_u32_e32 v192, s3, v207
	ds_read_b32 v208, v192
	v_or_b32_e32 v192, 0x200, v207
	v_add_u32_e32 v209, s3, v192
	v_or_b32_e32 v213, 0x400, v207
	v_add_u32_e32 v192, s95, v192
	ds_read_b32 v210, v209
	ds_read_b32 v211, v192
	v_add_u32_e32 v209, s3, v213
	v_or_b32_e32 v215, 0x600, v207
	v_add_u32_e32 v192, s95, v213
	ds_read_b32 v212, v209
	ds_read_b32 v213, v192
	v_add_u32_e32 v209, s3, v215
	v_add_u32_e32 v192, s95, v215
	s_add_i32 s4, 0, 0x19e00
	ds_read_b32 v214, v209
	ds_read_b32 v215, v192
	v_add_u32_e32 v209, s2, v207
	v_add_u32_e32 v192, s4, v207
	ds_read_b32 v216, v209
	ds_read_b32 v192, v192
	v_add_u32_e32 v209, s95, v207
	ds_read_b32 v209, v209
	s_waitcnt lgkmcnt(1)
	v_max_f32_e32 v192, v192, v192
	s_waitcnt lgkmcnt(0)
	v_pk_add_f32 v[208:209], v[208:209], v[210:211]
	v_pk_add_f32 v[210:211], v[212:213], v[214:215]
	s_nop 0
	v_pk_add_f32 v[208:209], v[208:209], v[210:211]
	s_nop 0
	v_fmac_f32_e32 v208, v216, v209
	v_max_f32_e64 v192, |v208|, v192
	v_div_scale_f32 v208, s[44:45], v192, v192, 1.0
	v_rcp_f32_e32 v209, v208
	s_nop 0
	v_fma_f32 v210, -v208, v209, 1.0
	v_fmac_f32_e32 v209, v210, v209
	v_div_scale_f32 v210, vcc, 1.0, v192, 1.0
	v_mul_f32_e32 v211, v210, v209
	v_fma_f32 v212, -v208, v211, v210
	v_fmac_f32_e32 v211, v212, v209
	v_fma_f32 v208, -v208, v211, v210
	v_div_fmas_f32 v208, v208, v209, v211
	v_div_fixup_f32 v208, v208, v192, 1.0
	v_or_b32_e32 v192, s40, v206
	v_lshlrev_b32_e32 v192, 11, v192
	v_pk_mul_f32 v[112:113], v[112:113], v[208:209] op_sel_hi:[1,0]
	v_pk_mul_f32 v[114:115], v[114:115], v[208:209] op_sel_hi:[1,0]
	v_lshl_add_u64 v[210:211], v[196:197], 0, v[192:193]
	v_cvt_pk_bf16_f32 v244, v112, v113
	v_cvt_pk_bf16_f32 v245, v114, v115
	v_pk_mul_f32 v[112:113], v[116:117], v[208:209] op_sel_hi:[1,0]
	v_pk_mul_f32 v[114:115], v[118:119], v[208:209] op_sel_hi:[1,0]
	v_cvt_pk_bf16_f32 v248, v112, v113
	v_cvt_pk_bf16_f32 v249, v114, v115
	v_pk_mul_f32 v[112:113], v[120:121], v[208:209] op_sel_hi:[1,0]
	v_pk_mul_f32 v[114:115], v[122:123], v[208:209] op_sel_hi:[1,0]
	v_cvt_pk_bf16_f32 v246, v112, v113
	v_cvt_pk_bf16_f32 v247, v114, v115
	v_pk_mul_f32 v[112:113], v[124:125], v[208:209] op_sel_hi:[1,0]
	v_pk_mul_f32 v[114:115], v[126:127], v[208:209] op_sel_hi:[1,0]
	v_or_b32_e32 v120, 32, v206
	v_cvt_pk_bf16_f32 v250, v112, v113
	v_cvt_pk_bf16_f32 v251, v114, v115
	v_lshlrev_b32_e32 v121, 2, v120
	v_or_b32_e32 v115, 0x280, v207
	v_mbcnt_lo_u32_b32 v252, -1, 0
	v_mbcnt_hi_u32_b32 v252, -1, v252
	v_lshrrev_b32_e32 v252, 5, v252
	v_mul_u32_u24_e32 v252, 24, v252
	v_mov_b32_e32 v253, 0
	v_permlane32_swap_b32_e32 v244, v246
	v_permlane32_swap_b32_e32 v245, v247
	v_permlane32_swap_b32_e32 v248, v250
	v_permlane32_swap_b32_e32 v249, v251
	v_lshl_add_u64 v[252:253], v[210:211], 0, v[252:253]
	global_store_dwordx4 v[252:253], v[244:247], off
	global_store_dwordx4 v[252:253], v[248:251], off offset:16
	v_add_u32_e32 v112, s3, v121
	v_add_u32_e32 v113, s3, v115
	v_or_b32_e32 v117, 0x480, v207
	v_add_u32_e32 v115, s95, v115
	ds_read_b32 v112, v112
	ds_read_b32 v114, v113
	ds_read_b32 v115, v115
	v_add_u32_e32 v113, s3, v117
	v_or_b32_e32 v119, 0x680, v207
	v_add_u32_e32 v117, s95, v117
	ds_read_b32 v116, v113
	ds_read_b32 v117, v117
	v_add_u32_e32 v113, s3, v119
	v_add_u32_e32 v119, s95, v119
	ds_read_b32 v118, v113
	ds_read_b32 v119, v119
	v_add_u32_e32 v113, s2, v121
	ds_read_b32 v122, v113
	v_add_u32_e32 v113, s95, v121
	ds_read_b32 v113, v113
	s_waitcnt lgkmcnt(0)
; DI unsigned pk2(float a, float b) { f32x2 f = {a, b}; bf16x2_t h = __builtin_convertvector(f, bf16x2_t); return __builtin_bit_cast(unsigned, h); }
; template <bool PASS2, int DIRT>
; DI void mlstm_item(const Params& P, LAS unsigned char* lds, int st, int g) {
;     ...
;             for (int jt = 0; jt < 4; ++jt) { const int j = 32 * jt + r;
;                 const float den = (sDENP[j] + sDENP[128 + j]) + (sDENP[256 + j] + sDENP[384 + j]) + sWST[j] * ((sQNP[j] + sQNP[128 + j]) + (sQNP[256 + j] + sQNP[384 + j]));
;                 const float inv = 1.0f / fmaxf(fabsf(den), sCL[j]);
;                 bf16_t* hp = Hd + (size_t)(tok0 + j) * 1024 + h * 256 + 32 * wid + 4 * hh;
; #pragma unroll
;                 for (int gq = 0; gq < 4; ++gq) { u32x2 w; w.x = pk2(num[jt][4 * gq] * inv, num[jt][4 * gq + 1] * inv); w.y = pk2(num[jt][4 * gq + 2] * inv, num[jt][4 * gq + 3] * inv); *(u32x2*)(hp + 8 * gq) = w; } }
	v_pk_add_f32 v[112:113], v[112:113], v[114:115]
	v_pk_add_f32 v[114:115], v[116:117], v[118:119]
	s_nop 0
	v_pk_add_f32 v[112:113], v[112:113], v[114:115]
	s_nop 0
	v_fmac_f32_e32 v112, v122, v113
	v_add_u32_e32 v113, s4, v121
	ds_read_b32 v113, v113
	s_waitcnt lgkmcnt(0)
	v_max_f32_e32 v113, v113, v113
	v_max_f32_e64 v112, |v112|, v113
	v_div_scale_f32 v113, s[44:45], v112, v112, 1.0
	v_rcp_f32_e32 v114, v113
	s_nop 0
	v_fma_f32 v115, -v113, v114, 1.0
	v_fmac_f32_e32 v114, v115, v114
	v_div_scale_f32 v115, vcc, 1.0, v112, 1.0
	v_mul_f32_e32 v116, v115, v114
	v_fma_f32 v117, -v113, v116, v115
	v_fmac_f32_e32 v116, v117, v114
	v_fma_f32 v113, -v113, v116, v115
	v_div_fmas_f32 v113, v113, v114, v116
	v_div_fixup_f32 v112, v113, v112, 1.0
	v_or_b32_e32 v113, s40, v120
	v_lshlrev_b32_e32 v192, 11, v113
	v_pk_mul_f32 v[96:97], v[96:97], v[112:113] op_sel_hi:[1,0]
	v_pk_mul_f32 v[98:99], v[98:99], v[112:113] op_sel_hi:[1,0]
	v_lshl_add_u64 v[114:115], v[196:197], 0, v[192:193]
	v_cvt_pk_bf16_f32 v244, v96, v97
	v_cvt_pk_bf16_f32 v245, v98, v99
	v_pk_mul_f32 v[96:97], v[100:101], v[112:113] op_sel_hi:[1,0]
	v_pk_mul_f32 v[98:99], v[102:103], v[112:113] op_sel_hi:[1,0]
	v_cvt_pk_bf16_f32 v248, v96, v97
	v_cvt_pk_bf16_f32 v249, v98, v99
	v_pk_mul_f32 v[96:97], v[104:105], v[112:113] op_sel_hi:[1,0]
	v_pk_mul_f32 v[98:99], v[106:107], v[112:113] op_sel_hi:[1,0]
	v_cvt_pk_bf16_f32 v246, v96, v97
	v_cvt_pk_bf16_f32 v247, v98, v99
	v_pk_mul_f32 v[96:97], v[108:109], v[112:113] op_sel_hi:[1,0]
	v_pk_mul_f32 v[98:99], v[110:111], v[112:113] op_sel_hi:[1,0]
	v_or_b32_e32 v104, 64, v206
	v_cvt_pk_bf16_f32 v250, v96, v97
	v_cvt_pk_bf16_f32 v251, v98, v99
	v_lshlrev_b32_e32 v105, 2, v104
	v_or_b32_e32 v99, 0x300, v207
	v_mbcnt_lo_u32_b32 v252, -1, 0
	v_mbcnt_hi_u32_b32 v252, -1, v252
	v_lshrrev_b32_e32 v252, 5, v252
	v_mul_u32_u24_e32 v252, 24, v252
	v_mov_b32_e32 v253, 0
	v_permlane32_swap_b32_e32 v244, v246
	v_permlane32_swap_b32_e32 v245, v247
	v_permlane32_swap_b32_e32 v248, v250
	v_permlane32_swap_b32_e32 v249, v251
	v_lshl_add_u64 v[252:253], v[114:115], 0, v[252:253]
	global_store_dwordx4 v[252:253], v[244:247], off
	global_store_dwordx4 v[252:253], v[248:251], off offset:16
	v_add_u32_e32 v96, s3, v105
	v_add_u32_e32 v97, s3, v99
	v_or_b32_e32 v101, 0x500, v207
	v_add_u32_e32 v99, s95, v99
	ds_read_b32 v96, v96
	ds_read_b32 v98, v97
	ds_read_b32 v99, v99
	v_add_u32_e32 v97, s3, v101
	v_or_b32_e32 v103, 0x700, v207
	v_add_u32_e32 v101, s95, v101
	ds_read_b32 v100, v97
	ds_read_b32 v101, v101
	v_add_u32_e32 v97, s3, v103
	v_add_u32_e32 v103, s95, v103
	ds_read_b32 v102, v97
	ds_read_b32 v103, v103
	v_add_u32_e32 v97, s2, v105
	ds_read_b32 v106, v97
	v_add_u32_e32 v97, s95, v105
	ds_read_b32 v97, v97
	s_waitcnt lgkmcnt(0)
	v_pk_add_f32 v[96:97], v[96:97], v[98:99]
	v_pk_add_f32 v[98:99], v[100:101], v[102:103]
	s_nop 0
	v_pk_add_f32 v[96:97], v[96:97], v[98:99]
	s_nop 0
	v_fmac_f32_e32 v96, v106, v97
	v_add_u32_e32 v97, s4, v105
	ds_read_b32 v97, v97
	s_waitcnt lgkmcnt(0)
	v_max_f32_e32 v97, v97, v97
	v_max_f32_e64 v96, |v96|, v97
	v_div_scale_f32 v97, s[44:45], v96, v96, 1.0
	v_rcp_f32_e32 v98, v97
	s_nop 0
	v_fma_f32 v99, -v97, v98, 1.0
	v_fmac_f32_e32 v98, v99, v98
	v_div_scale_f32 v99, vcc, 1.0, v96, 1.0
	v_mul_f32_e32 v100, v99, v98
	v_fma_f32 v101, -v97, v100, v99
	v_fmac_f32_e32 v100, v101, v98
	v_fma_f32 v97, -v97, v100, v99
	v_div_fmas_f32 v97, v97, v98, v100
	v_div_fixup_f32 v96, v97, v96, 1.0
	v_or_b32_e32 v97, s40, v104
	v_lshlrev_b32_e32 v192, 11, v97
	v_pk_mul_f32 v[80:81], v[80:81], v[96:97] op_sel_hi:[1,0]
	v_pk_mul_f32 v[82:83], v[82:83], v[96:97] op_sel_hi:[1,0]
	v_lshl_add_u64 v[98:99], v[196:197], 0, v[192:193]
	v_cvt_pk_bf16_f32 v244, v80, v81
	v_cvt_pk_bf16_f32 v245, v82, v83
	v_pk_mul_f32 v[80:81], v[84:85], v[96:97] op_sel_hi:[1,0]
	v_pk_mul_f32 v[82:83], v[86:87], v[96:97] op_sel_hi:[1,0]
	v_cvt_pk_bf16_f32 v248, v80, v81
	v_cvt_pk_bf16_f32 v249, v82, v83
	v_pk_mul_f32 v[80:81], v[88:89], v[96:97] op_sel_hi:[1,0]
	v_pk_mul_f32 v[82:83], v[90:91], v[96:97] op_sel_hi:[1,0]
	v_cvt_pk_bf16_f32 v246, v80, v81
	v_cvt_pk_bf16_f32 v247, v82, v83
	v_pk_mul_f32 v[80:81], v[92:93], v[96:97] op_sel_hi:[1,0]
	v_pk_mul_f32 v[82:83], v[94:95], v[96:97] op_sel_hi:[1,0]
	v_or_b32_e32 v88, 0x60, v206
	v_cvt_pk_bf16_f32 v250, v80, v81
	v_cvt_pk_bf16_f32 v251, v82, v83
	v_lshlrev_b32_e32 v89, 2, v88
	v_or_b32_e32 v83, 0x380, v207
	v_mbcnt_lo_u32_b32 v252, -1, 0
	v_mbcnt_hi_u32_b32 v252, -1, v252
	v_lshrrev_b32_e32 v252, 5, v252
	v_mul_u32_u24_e32 v252, 24, v252
	v_mov_b32_e32 v253, 0
	v_permlane32_swap_b32_e32 v244, v246
	v_permlane32_swap_b32_e32 v245, v247
	v_permlane32_swap_b32_e32 v248, v250
	v_permlane32_swap_b32_e32 v249, v251
	v_lshl_add_u64 v[252:253], v[98:99], 0, v[252:253]
	global_store_dwordx4 v[252:253], v[244:247], off
	global_store_dwordx4 v[252:253], v[248:251], off offset:16
	v_add_u32_e32 v80, s3, v89
	v_add_u32_e32 v81, s3, v83
	v_or_b32_e32 v85, 0x580, v207
	v_add_u32_e32 v83, s95, v83
	ds_read_b32 v80, v80
	ds_read_b32 v82, v81
	ds_read_b32 v83, v83
	v_add_u32_e32 v81, s3, v85
	v_or_b32_e32 v87, 0x780, v207
	v_add_u32_e32 v85, s95, v85
	ds_read_b32 v84, v81
	ds_read_b32 v85, v85
	v_add_u32_e32 v81, s3, v87
	v_add_u32_e32 v87, s95, v87
	ds_read_b32 v86, v81
	ds_read_b32 v87, v87
	v_add_u32_e32 v81, s2, v89
	ds_read_b32 v90, v81
	v_add_u32_e32 v81, s95, v89
	ds_read_b32 v81, v81
	s_waitcnt lgkmcnt(0)
; DI int lane_id() { int l; asm volatile("v_mbcnt_lo_u32_b32 %0, -1, 0\n\tv_mbcnt_hi_u32_b32 %0, -1, %0" : "=v"(l)); return l; }
; DI unsigned pk2(float a, float b) { f32x2 f = {a, b}; bf16x2_t h = __builtin_convertvector(f, bf16x2_t); return __builtin_bit_cast(unsigned, h); }
; template <bool PASS2, int DIRT>
; DI void mlstm_item(const Params& P, LAS unsigned char* lds, int st, int g) {
;     ...
;             for (int jt = 0; jt < 4; ++jt) { const int j = 32 * jt + r;
;                 const float den = (sDENP[j] + sDENP[128 + j]) + (sDENP[256 + j] + sDENP[384 + j]) + sWST[j] * ((sQNP[j] + sQNP[128 + j]) + (sQNP[256 + j] + sQNP[384 + j]));
;                 const float inv = 1.0f / fmaxf(fabsf(den), sCL[j]);
;                 bf16_t* hp = Hd + (size_t)(tok0 + j) * 1024 + h * 256 + 32 * wid + 4 * hh;
; #pragma unroll
;                 for (int gq = 0; gq < 4; ++gq) { u32x2 w; w.x = pk2(num[jt][4 * gq] * inv, num[jt][4 * gq + 1] * inv); w.y = pk2(num[jt][4 * gq + 2] * inv, num[jt][4 * gq + 3] * inv); *(u32x2*)(hp + 8 * gq) = w; } }
;         }
;         tid = (wid << 6) | lane_id(); asm volatile("" : "+v"(tid)); lane = tid & 63; r = lane & 31; hh = lane >> 5;
;         if (ci + 1 < nchunks) { const int tokn = chunk_tok0(ci + 1);
; #pragma unroll
;             for (int i = 0; i < 4; ++i) { const int n = tid + 512 * i, row = n >> 4, ch = n & 15; kq[i] = *(const u32x4*)(Kg + (size_t)(tokn + row) * 512 + h * 128 + ch * 8);
;                 if (PASS2) kq[4 + i] = *(const u32x4*)(Qg + (size_t)(tokn + row) * 512 + h * 128 + ch * 8); } }
	v_pk_add_f32 v[80:81], v[80:81], v[82:83]
	v_pk_add_f32 v[82:83], v[84:85], v[86:87]
	s_nop 0
	v_pk_add_f32 v[80:81], v[80:81], v[82:83]
	s_nop 0
	v_fmac_f32_e32 v80, v90, v81
	v_add_u32_e32 v81, s4, v89
	ds_read_b32 v81, v81
	s_add_i32 s4, s72, 1
	s_cmp_lg_u32 s72, 7
	s_waitcnt lgkmcnt(0)
	v_max_f32_e32 v81, v81, v81
	v_max_f32_e64 v80, |v80|, v81
	v_div_scale_f32 v81, s[2:3], v80, v80, 1.0
	v_rcp_f32_e32 v82, v81
	s_mov_b64 s[2:3], -1
	v_fma_f32 v83, -v81, v82, 1.0
	v_fmac_f32_e32 v82, v83, v82
	v_div_scale_f32 v83, vcc, 1.0, v80, 1.0
	v_mul_f32_e32 v84, v83, v82
	v_fma_f32 v85, -v81, v84, v83
	v_fmac_f32_e32 v84, v85, v82
	v_fma_f32 v81, -v81, v84, v83
	v_div_fmas_f32 v81, v81, v82, v84
	v_div_fixup_f32 v80, v81, v80, 1.0
	v_or_b32_e32 v81, s40, v88
	v_lshlrev_b32_e32 v192, 11, v81
	v_pk_mul_f32 v[64:65], v[64:65], v[80:81] op_sel_hi:[1,0]
	v_pk_mul_f32 v[66:67], v[66:67], v[80:81] op_sel_hi:[1,0]
	v_lshl_add_u64 v[82:83], v[196:197], 0, v[192:193]
	v_cvt_pk_bf16_f32 v244, v64, v65
	v_cvt_pk_bf16_f32 v245, v66, v67
	v_pk_mul_f32 v[64:65], v[68:69], v[80:81] op_sel_hi:[1,0]
	v_pk_mul_f32 v[66:67], v[70:71], v[80:81] op_sel_hi:[1,0]
	v_cvt_pk_bf16_f32 v248, v64, v65
	v_cvt_pk_bf16_f32 v249, v66, v67
	v_pk_mul_f32 v[64:65], v[72:73], v[80:81] op_sel_hi:[1,0]
	v_pk_mul_f32 v[66:67], v[74:75], v[80:81] op_sel_hi:[1,0]
	v_cvt_pk_bf16_f32 v246, v64, v65
	v_cvt_pk_bf16_f32 v247, v66, v67
	v_pk_mul_f32 v[64:65], v[76:77], v[80:81] op_sel_hi:[1,0]
	v_pk_mul_f32 v[66:67], v[78:79], v[80:81] op_sel_hi:[1,0]
	v_cvt_pk_bf16_f32 v250, v64, v65
	v_cvt_pk_bf16_f32 v251, v66, v67
	v_mbcnt_lo_u32_b32 v252, -1, 0
	v_mbcnt_hi_u32_b32 v252, -1, v252
	v_lshrrev_b32_e32 v252, 5, v252
	v_mul_u32_u24_e32 v252, 24, v252
	v_mov_b32_e32 v253, 0
	v_permlane32_swap_b32_e32 v244, v246
	v_permlane32_swap_b32_e32 v245, v247
	v_permlane32_swap_b32_e32 v248, v250
	v_permlane32_swap_b32_e32 v249, v251
	v_lshl_add_u64 v[252:253], v[82:83], 0, v[252:253]
	global_store_dwordx4 v[252:253], v[244:247], off
	global_store_dwordx4 v[252:253], v[248:251], off offset:16
	v_mbcnt_lo_u32_b32 v64, -1, 0
	v_mbcnt_hi_u32_b32 v64, -1, v64
	s_nop 0
	v_or_b32_e32 v97, s97, v64
	s_nop 0
	v_lshlrev_b32_e32 v96, 3, v97
	s_cbranch_scc0 .LBB0_759
	s_lshl_b32 s2, s4, 7
	v_lshlrev_b32_e32 v64, 4, v97
	v_add_u32_e32 v72, 0x200, v97
	v_add_u32_e32 v80, 0x400, v97
	v_add_u32_e32 v92, 0x600, v97
	s_sub_i32 s2, s43, s2
	v_and_b32_e32 v192, 0xf0, v64
	v_ashrrev_i32_e32 v64, 4, v97
	v_ashrrev_i32_e32 v72, 4, v72
	v_ashrrev_i32_e32 v80, 4, v80
	v_ashrrev_i32_e32 v92, 4, v92
	v_add_u32_e32 v64, s2, v64
	v_add_u32_e32 v72, s2, v72
	v_add_u32_e32 v80, s2, v80
	v_add_u32_e32 v92, s2, v92
	v_ashrrev_i32_e32 v65, 31, v64
	v_ashrrev_i32_e32 v73, 31, v72
	v_ashrrev_i32_e32 v81, 31, v80
	v_ashrrev_i32_e32 v93, 31, v92
	v_lshl_add_u64 v[88:89], s[6:7], 0, v[192:193]
	v_lshl_add_u64 v[90:91], s[8:9], 0, v[192:193]
	v_lshlrev_b64 v[64:65], 10, v[64:65]
	v_lshlrev_b64 v[72:73], 10, v[72:73]
	v_lshlrev_b64 v[80:81], 10, v[80:81]
	v_lshlrev_b64 v[92:93], 10, v[92:93]
	v_lshl_add_u64 v[66:67], v[88:89], 0, v[64:65]
	v_lshl_add_u64 v[64:65], v[90:91], 0, v[64:65]
	v_lshl_add_u64 v[74:75], v[88:89], 0, v[72:73]
	v_lshl_add_u64 v[72:73], v[90:91], 0, v[72:73]
	v_lshl_add_u64 v[82:83], v[88:89], 0, v[80:81]
	v_lshl_add_u64 v[80:81], v[90:91], 0, v[80:81]
	v_lshl_add_u64 v[88:89], v[88:89], 0, v[92:93]
	v_lshl_add_u64 v[90:91], v[90:91], 0, v[92:93]
	global_load_dwordx4 v[68:71], v[66:67], off
	s_nop 0
	global_load_dwordx4 v[64:67], v[64:65], off
	s_nop 0
	global_load_dwordx4 v[76:79], v[74:75], off
	s_nop 0
	global_load_dwordx4 v[72:75], v[72:73], off
	s_nop 0
	global_load_dwordx4 v[84:87], v[82:83], off
	s_nop 0
	global_load_dwordx4 v[80:83], v[80:81], off
	s_nop 0
	global_load_dwordx4 v[92:95], v[88:89], off
	s_nop 0
	global_load_dwordx4 v[88:91], v[90:91], off
	v_lshlrev_b32_e32 v98, 3, v97
	s_mov_b64 s[2:3], 0

; #define LAS __attribute__((address_space(3)))
; template <bool PASS2, int DIRT>
; DI void mlstm_item(const Params& P, LAS unsigned char* lds, int st, int g) {
;     ...
;             { const int j = tid & 127, part = tid >> 7; float s = 0.f;
; #pragma unroll
;               for (int cc = 0; cc < 4; ++cc) { const u32x4 q8 = *(const LAS u32x4*)(QS + off_b(j, 4 * part + cc)); const f32x4 n0a = *(const LAS f32x4*)(sN0 + 32 * part + 8 * cc), n0b = *(const LAS f32x4*)(sN0 + 32 * part + 8 * cc + 4);
;                   s += bf_lo(q8.x) * n0a[0] + bf_hi(q8.x) * n0a[1] + bf_lo(q8.y) * n0a[2] + bf_hi(q8.y) * n0a[3] + bf_lo(q8.z) * n0b[0] + bf_hi(q8.z) * n0b[1] + bf_lo(q8.w) * n0b[2] + bf_hi(q8.w) * n0b[3]; }
;               sQNP[part * 128 + j] = s; }
;             tid = (wid << 6) | lane_id(); asm volatile("" : "+v"(tid)); lane = tid & 63; r = lane & 31; hh = lane >> 5;
; #pragma unroll
;             for (int jt = 0; jt < 4; ++jt)
; #pragma unroll
;                 for (int e = 0; e < 16; ++e) num[jt][e] = 0.f;
;             {
;                 bf16x8 qf[2][4];
;                 auto ldq = [&](int g_, bf16x8 (&qb)[4]) { const int dkt = g_ >> 1, s2 = g_ & 1;
; #pragma unroll
;                     for (int jt = 0; jt < 4; ++jt) { const s16x4 lo = *(const LAS s16x4*)(QS + off_b(32 * jt + r, 4 * dkt + 2 * s2) + 8 * hh); const s16x4 hi = *(const LAS s16x4*)(QS + off_b(32 * jt + r, 4 * dkt + 2 * s2 + 1) + 8 * hh);
;                         qb[jt] = __builtin_shufflevector(lo, hi, 0, 1, 2, 3, 4, 5, 6, 7); } };
;                 ldq(0, qf[0]);
; #pragma unroll
;                 for (int g_ = 0; g_ < 8; ++g_) { const int dkt = g_ >> 1, s2 = g_ & 1;
;                     if (g_ + 1 < 8) ldq(g_ + 1, qf[(g_ + 1) & 1]);
;                     __builtin_amdgcn_sched_barrier(0);
;                     u32x4 xp; xp.x = pk2(C[dkt][8 * s2 + 0], C[dkt][8 * s2 + 1]); xp.y = pk2(C[dkt][8 * s2 + 2], C[dkt][8 * s2 + 3]); xp.z = pk2(C[dkt][8 * s2 + 4], C[dkt][8 * s2 + 5]); xp.w = pk2(C[dkt][8 * s2 + 6], C[dkt][8 * s2 + 7]);
;                     const bf16x8 xs = __builtin_bit_cast(bf16x8, xp);
; #pragma unroll
;                     for (int jt = 0; jt < 4; ++jt) num[jt] = MFMA32(xs, qf[g_ & 1][jt], num[jt]);
;                     __builtin_amdgcn_sched_barrier(0);
;                     if (s2 == 1) asm volatile("" : "+v"(num[0]), "+v"(num[1]), "+v"(num[2]), "+v"(num[3]) :: "memory"); }
.LBB0_808:
	s_and_saveexec_b64 s[4:5], s[2:3]
	v_lshl_add_u32 v65, v90, 2, s1
	ds_write_b32 v65, v64
	s_or_b64 exec, exec, s[4:5]
	v_and_b32_e32 v65, 0xffffff80, v80
	v_add_u32_e32 v65, 0, v65
	v_and_b32_e32 v64, 0x7f, v80
	v_add_u32_e32 v81, 0x1a600, v65
	v_ashrrev_i32_e32 v65, 1, v80
	v_mul_u32_u24_e32 v64, 0x110, v64
	v_and_b32_e32 v65, 0xffffffc0, v65
	v_add3_u32 v76, 0, v64, v65
	s_waitcnt lgkmcnt(1)
	ds_read_b128 v[64:67], v76
	ds_read_b128 v[68:71], v76 offset:16
	ds_read_b128 v[72:75], v76 offset:32
	ds_read_b128 v[76:79], v76 offset:48
	ds_read_b128 v[82:85], v81
	ds_read_b128 v[86:89], v81 offset:16
	ds_read_b128 v[90:93], v81 offset:32
	ds_read_b128 v[94:97], v81 offset:48
	s_waitcnt lgkmcnt(6)
	v_and_b32_e32 v103, 0xffff0000, v68
	v_and_b32_e32 v102, 0xffff0000, v64
	v_lshlrev_b32_e32 v99, 16, v68
	s_waitcnt lgkmcnt(1)
	v_mov_b32_e32 v101, v90
	v_mov_b32_e32 v90, v83
	v_lshlrev_b32_e32 v98, 16, v64
	v_mov_b32_e32 v100, v82
	v_pk_mul_f32 v[82:83], v[90:91], v[102:103]
	v_lshlrev_b32_e32 v91, 16, v69
	v_pk_fma_f32 v[82:83], v[100:101], v[98:99], v[82:83]
	v_lshlrev_b32_e32 v90, 16, v65
	v_mov_b32_e32 v98, v84
	v_mov_b32_e32 v99, v92
	v_pk_fma_f32 v[82:83], v[98:99], v[90:91], v[82:83]
	v_and_b32_e32 v69, 0xffff0000, v69
	v_and_b32_e32 v68, 0xffff0000, v65
	v_mov_b32_e32 v92, v85
	v_pk_fma_f32 v[64:65], v[92:93], v[68:69], v[82:83]
	v_lshlrev_b32_e32 v69, 16, v70
	v_lshlrev_b32_e32 v68, 16, v66
	v_mov_b32_e32 v82, v86
	s_waitcnt lgkmcnt(0)
	v_mov_b32_e32 v83, v94
	v_pk_fma_f32 v[64:65], v[82:83], v[68:69], v[64:65]
	v_and_b32_e32 v69, 0xffff0000, v70
	v_and_b32_e32 v68, 0xffff0000, v66
	v_mov_b32_e32 v94, v87
	v_pk_fma_f32 v[64:65], v[94:95], v[68:69], v[64:65]
	v_lshlrev_b32_e32 v69, 16, v71
	v_lshlrev_b32_e32 v68, 16, v67
	v_mov_b32_e32 v82, v88
	v_mov_b32_e32 v83, v96
	v_pk_fma_f32 v[64:65], v[82:83], v[68:69], v[64:65]
	v_and_b32_e32 v69, 0xffff0000, v71
	v_and_b32_e32 v68, 0xffff0000, v67
	v_mov_b32_e32 v96, v89
	v_pk_fma_f32 v[64:65], v[96:97], v[68:69], v[64:65]
	v_and_b32_e32 v95, 0xffff0000, v76
	v_add_f32_e32 v64, 0, v64
	v_add_f32_e32 v96, v64, v65
	ds_read_b128 v[64:67], v81 offset:64
	ds_read_b128 v[68:71], v81 offset:80
	ds_read_b128 v[82:85], v81 offset:96
	ds_read_b128 v[86:89], v81 offset:112
	v_and_b32_e32 v94, 0xffff0000, v72
	v_lshlrev_b32_e32 v91, 16, v76
	v_lshlrev_b32_e32 v90, 16, v72
	s_waitcnt lgkmcnt(1)
	v_mov_b32_e32 v93, v82
	v_mov_b32_e32 v82, v65
	v_mov_b32_e32 v92, v64
	v_pk_mul_f32 v[64:65], v[82:83], v[94:95]
	v_lshlrev_b32_e32 v83, 16, v77
	v_pk_fma_f32 v[64:65], v[92:93], v[90:91], v[64:65]
	v_lshlrev_b32_e32 v82, 16, v73
	v_mov_b32_e32 v90, v66
	v_mov_b32_e32 v91, v84
	v_pk_fma_f32 v[64:65], v[90:91], v[82:83], v[64:65]
	v_and_b32_e32 v77, 0xffff0000, v77
	v_and_b32_e32 v76, 0xffff0000, v73
	v_mov_b32_e32 v84, v67
	v_pk_fma_f32 v[64:65], v[84:85], v[76:77], v[64:65]
	v_lshlrev_b32_e32 v67, 16, v78
	v_lshlrev_b32_e32 v66, 16, v74
	v_mov_b32_e32 v72, v68
	s_waitcnt lgkmcnt(0)
	v_mov_b32_e32 v73, v86
	v_pk_fma_f32 v[64:65], v[72:73], v[66:67], v[64:65]
	v_and_b32_e32 v67, 0xffff0000, v78
	v_and_b32_e32 v66, 0xffff0000, v74
	v_mov_b32_e32 v86, v69
	v_pk_fma_f32 v[64:65], v[86:87], v[66:67], v[64:65]
	v_lshlrev_b32_e32 v67, 16, v79
	v_lshlrev_b32_e32 v66, 16, v75
	v_mov_b32_e32 v68, v70
	v_mov_b32_e32 v69, v88
	v_pk_fma_f32 v[64:65], v[68:69], v[66:67], v[64:65]
	v_and_b32_e32 v67, 0xffff0000, v79
	v_and_b32_e32 v66, 0xffff0000, v75
	v_mov_b32_e32 v88, v71
	v_pk_fma_f32 v[64:65], v[88:89], v[66:67], v[64:65]
	s_nop 0
	v_add_f32_e32 v64, v96, v64
	v_add_f32_e32 v64, v64, v65
	v_lshl_add_u32 v65, v80, 2, s95
	ds_write_b32 v65, v64
	v_mbcnt_lo_u32_b32 v64, -1, 0
	v_mbcnt_hi_u32_b32 v64, -1, v64
	s_nop 0
	v_or_b32_e32 v64, s97, v64
	s_nop 0
	v_and_b32_e32 v192, 31, v64
	v_lshrrev_b32_e32 v64, 2, v64
	v_mul_u32_u24_e32 v65, 0x110, v192
	v_and_b32_e32 v64, 8, v64
	v_add3_u32 v195, 0, v65, v64
	v_add_u32_e32 v196, 0x2000, v195
	v_add_u32_e32 v197, 0x4000, v195
	v_add_u32_e32 v242, 0x6000, v195
	ds_read2_b64 v[64:67], v195 offset1:2
	ds_read2_b64 v[206:209], v195 offset0:4 offset1:6
	ds_read2_b64 v[68:71], v196 offset0:64 offset1:66
	ds_read2_b64 v[72:75], v197 offset0:128 offset1:130
	ds_read2_b64 v[76:79], v242 offset0:192 offset1:194
	ds_read2_b64 v[210:213], v196 offset0:68 offset1:70
	ds_read2_b64 v[214:217], v197 offset0:132 offset1:134
	ds_read2_b64 v[218:221], v242 offset0:196 offset1:198
	v_cvt_pk_bf16_f32 v222, v0, v1
	v_cvt_pk_bf16_f32 v223, v2, v3
	v_cvt_pk_bf16_f32 v224, v4, v5
	v_cvt_pk_bf16_f32 v225, v6, v7
	s_waitcnt lgkmcnt(7)
	s_nop 0
	v_mfma_f32_32x32x16_bf16 v[112:127], v[222:225], v[64:67], 0
	s_waitcnt lgkmcnt(5)
	v_mfma_f32_32x32x16_bf16 v[96:111], v[222:225], v[68:71], 0
	s_waitcnt lgkmcnt(4)
	v_mfma_f32_32x32x16_bf16 v[80:95], v[222:225], v[72:75], 0
	s_waitcnt lgkmcnt(3)
	v_mfma_f32_32x32x16_bf16 v[64:79], v[222:225], v[76:79], 0
	ds_read2_b64 v[222:225], v195 offset0:8 offset1:10
	ds_read2_b64 v[226:229], v196 offset0:72 offset1:74
	ds_read2_b64 v[230:233], v197 offset0:136 offset1:138
	ds_read2_b64 v[234:237], v242 offset0:200 offset1:202
	v_cvt_pk_bf16_f32 v238, v8, v9
	v_cvt_pk_bf16_f32 v239, v10, v11
	v_cvt_pk_bf16_f32 v240, v12, v13
	v_cvt_pk_bf16_f32 v241, v14, v15
	s_waitcnt lgkmcnt(6)
	s_nop 0
	v_mfma_f32_32x32x16_bf16 v[96:111], v[238:241], v[210:213], v[96:111]
	s_waitcnt lgkmcnt(5)
	v_mfma_f32_32x32x16_bf16 v[80:95], v[238:241], v[214:217], v[80:95]
	s_waitcnt lgkmcnt(4)
; DI unsigned pk2(float a, float b) { f32x2 f = {a, b}; bf16x2_t h = __builtin_convertvector(f, bf16x2_t); return __builtin_bit_cast(unsigned, h); }
; #define MFMA32(a, b, c) __builtin_amdgcn_mfma_f32_32x32x16_bf16((a), (b), (c), 0, 0, 0)
; template <bool PASS2, int DIRT>
; DI void mlstm_item(const Params& P, LAS unsigned char* lds, int st, int g) {
;     ...
;                 for (int g_ = 0; g_ < 8; ++g_) { const int dkt = g_ >> 1, s2 = g_ & 1;
;                     if (g_ + 1 < 8) ldq(g_ + 1, qf[(g_ + 1) & 1]);
;                     __builtin_amdgcn_sched_barrier(0);
;                     u32x4 xp; xp.x = pk2(C[dkt][8 * s2 + 0], C[dkt][8 * s2 + 1]); xp.y = pk2(C[dkt][8 * s2 + 2], C[dkt][8 * s2 + 3]); xp.z = pk2(C[dkt][8 * s2 + 4], C[dkt][8 * s2 + 5]); xp.w = pk2(C[dkt][8 * s2 + 6], C[dkt][8 * s2 + 7]);
;                     const bf16x8 xs = __builtin_bit_cast(bf16x8, xp);
; #pragma unroll
;                     for (int jt = 0; jt < 4; ++jt) num[jt] = MFMA32(xs, qf[g_ & 1][jt], num[jt]);
;                     __builtin_amdgcn_sched_barrier(0);
;                     if (s2 == 1) asm volatile("" : "+v"(num[0]), "+v"(num[1]), "+v"(num[2]), "+v"(num[3]) :: "memory"); }
;             }
; #pragma unroll
;             for (int jt = 0; jt < 4; ++jt) { const float ws_ = sWST[32 * jt + r];
; #pragma unroll
;                 for (int e = 0; e < 16; ++e) num[jt][e] *= ws_; }
;             __syncthreads();
	v_mfma_f32_32x32x16_bf16 v[64:79], v[238:241], v[218:221], v[64:79]
	v_mfma_f32_32x32x16_bf16 v[112:127], v[238:241], v[206:209], v[112:127]
	ds_read2_b64 v[206:209], v195 offset0:12 offset1:14
	ds_read2_b64 v[210:213], v196 offset0:76 offset1:78
	ds_read2_b64 v[214:217], v197 offset0:140 offset1:142
	ds_read2_b64 v[218:221], v242 offset0:204 offset1:206
	v_cvt_pk_bf16_f32 v238, v16, v17
	v_cvt_pk_bf16_f32 v239, v18, v19
	v_cvt_pk_bf16_f32 v240, v20, v21
	v_cvt_pk_bf16_f32 v241, v22, v23
	s_waitcnt lgkmcnt(6)
	s_nop 0
	v_mfma_f32_32x32x16_bf16 v[96:111], v[238:241], v[226:229], v[96:111]
	s_waitcnt lgkmcnt(5)
	v_mfma_f32_32x32x16_bf16 v[80:95], v[238:241], v[230:233], v[80:95]
	s_waitcnt lgkmcnt(4)
	v_mfma_f32_32x32x16_bf16 v[64:79], v[238:241], v[234:237], v[64:79]
	v_mfma_f32_32x32x16_bf16 v[112:127], v[238:241], v[222:225], v[112:127]
	ds_read2_b64 v[222:225], v195 offset0:16 offset1:18
	ds_read2_b64 v[226:229], v196 offset0:80 offset1:82
	ds_read2_b64 v[230:233], v197 offset0:144 offset1:146
	ds_read2_b64 v[234:237], v242 offset0:208 offset1:210
	v_cvt_pk_bf16_f32 v238, v24, v25
	v_cvt_pk_bf16_f32 v239, v26, v27
	v_cvt_pk_bf16_f32 v240, v28, v29
	v_cvt_pk_bf16_f32 v241, v30, v31
	s_waitcnt lgkmcnt(6)
	s_nop 0
	v_mfma_f32_32x32x16_bf16 v[96:111], v[238:241], v[210:213], v[96:111]
	s_waitcnt lgkmcnt(5)
	v_mfma_f32_32x32x16_bf16 v[80:95], v[238:241], v[214:217], v[80:95]
	s_waitcnt lgkmcnt(4)
	v_mfma_f32_32x32x16_bf16 v[64:79], v[238:241], v[218:221], v[64:79]
	v_mfma_f32_32x32x16_bf16 v[112:127], v[238:241], v[206:209], v[112:127]
	ds_read2_b64 v[206:209], v195 offset0:20 offset1:22
	ds_read2_b64 v[210:213], v196 offset0:84 offset1:86
	ds_read2_b64 v[214:217], v197 offset0:148 offset1:150
	ds_read2_b64 v[218:221], v242 offset0:212 offset1:214
	v_cvt_pk_bf16_f32 v238, v32, v33
	v_cvt_pk_bf16_f32 v239, v34, v35
	v_cvt_pk_bf16_f32 v240, v36, v37
	v_cvt_pk_bf16_f32 v241, v38, v39
	s_waitcnt lgkmcnt(6)
	s_nop 0
	v_mfma_f32_32x32x16_bf16 v[96:111], v[238:241], v[226:229], v[96:111]
	s_waitcnt lgkmcnt(5)
	v_mfma_f32_32x32x16_bf16 v[80:95], v[238:241], v[230:233], v[80:95]
	s_waitcnt lgkmcnt(4)
	v_mfma_f32_32x32x16_bf16 v[64:79], v[238:241], v[234:237], v[64:79]
	v_mfma_f32_32x32x16_bf16 v[112:127], v[238:241], v[222:225], v[112:127]
	ds_read2_b64 v[222:225], v195 offset0:24 offset1:26
	ds_read2_b64 v[226:229], v196 offset0:88 offset1:90
	ds_read2_b64 v[230:233], v197 offset0:152 offset1:154
	ds_read2_b64 v[234:237], v242 offset0:216 offset1:218
	v_cvt_pk_bf16_f32 v238, v40, v41
	v_cvt_pk_bf16_f32 v239, v42, v43
	v_cvt_pk_bf16_f32 v240, v44, v45
	v_cvt_pk_bf16_f32 v241, v46, v47
	s_waitcnt lgkmcnt(6)
	s_nop 0
	v_mfma_f32_32x32x16_bf16 v[96:111], v[238:241], v[210:213], v[96:111]
	s_waitcnt lgkmcnt(5)
	v_mfma_f32_32x32x16_bf16 v[80:95], v[238:241], v[214:217], v[80:95]
	s_waitcnt lgkmcnt(4)
	v_mfma_f32_32x32x16_bf16 v[64:79], v[238:241], v[218:221], v[64:79]
	v_mfma_f32_32x32x16_bf16 v[112:127], v[238:241], v[206:209], v[112:127]
	ds_read2_b64 v[206:209], v195 offset0:28 offset1:30
	ds_read2_b64 v[210:213], v196 offset0:92 offset1:94
	ds_read2_b64 v[214:217], v197 offset0:156 offset1:158
	ds_read2_b64 v[218:221], v242 offset0:220 offset1:222
	v_cvt_pk_bf16_f32 v238, v48, v49
	v_cvt_pk_bf16_f32 v239, v50, v51
	v_cvt_pk_bf16_f32 v240, v52, v53
	v_cvt_pk_bf16_f32 v241, v54, v55
	s_waitcnt lgkmcnt(6)
	s_nop 0
	v_mfma_f32_32x32x16_bf16 v[96:111], v[238:241], v[226:229], v[96:111]
	s_waitcnt lgkmcnt(5)
	v_mfma_f32_32x32x16_bf16 v[80:95], v[238:241], v[230:233], v[80:95]
	s_waitcnt lgkmcnt(4)
	v_mfma_f32_32x32x16_bf16 v[64:79], v[238:241], v[234:237], v[64:79]
	v_mfma_f32_32x32x16_bf16 v[112:127], v[238:241], v[222:225], v[112:127]
	v_cvt_pk_bf16_f32 v222, v56, v57
	v_cvt_pk_bf16_f32 v223, v58, v59
	v_cvt_pk_bf16_f32 v224, v60, v61
	v_cvt_pk_bf16_f32 v225, v62, v63
	s_waitcnt lgkmcnt(2)
	s_nop 0
	v_mfma_f32_32x32x16_bf16 v[96:111], v[222:225], v[210:213], v[96:111]
	s_waitcnt lgkmcnt(1)
	v_mfma_f32_32x32x16_bf16 v[80:95], v[222:225], v[214:217], v[80:95]
	s_waitcnt lgkmcnt(0)
	v_mfma_f32_32x32x16_bf16 v[64:79], v[222:225], v[218:221], v[64:79]
	v_mfma_f32_32x32x16_bf16 v[112:127], v[222:225], v[206:209], v[112:127]
	s_add_i32 s2, 0, 0x19c00
	v_lshl_add_u32 v195, v192, 2, s2
	ds_read2_b32 v[196:197], v195 offset1:32
	s_add_i32 s3, 0, 0x11000
	s_waitcnt lgkmcnt(0)
	s_nop 6
	v_pk_mul_f32 v[126:127], v[196:197], v[126:127] op_sel_hi:[0,1]
	v_pk_mul_f32 v[124:125], v[196:197], v[124:125] op_sel_hi:[0,1]
	v_pk_mul_f32 v[122:123], v[196:197], v[122:123] op_sel_hi:[0,1]
	v_pk_mul_f32 v[120:121], v[196:197], v[120:121] op_sel_hi:[0,1]
	v_pk_mul_f32 v[118:119], v[196:197], v[118:119] op_sel_hi:[0,1]
	v_pk_mul_f32 v[116:117], v[196:197], v[116:117] op_sel_hi:[0,1]
	v_pk_mul_f32 v[114:115], v[196:197], v[114:115] op_sel_hi:[0,1]
	v_pk_mul_f32 v[112:113], v[196:197], v[112:113] op_sel_hi:[0,1]
	v_mov_b32_e32 v192, v197
	ds_read2_b32 v[196:197], v195 offset0:64 offset1:96
	v_pk_mul_f32 v[110:111], v[192:193], v[110:111] op_sel_hi:[0,1]
	v_pk_mul_f32 v[108:109], v[192:193], v[108:109] op_sel_hi:[0,1]
	v_pk_mul_f32 v[106:107], v[192:193], v[106:107] op_sel_hi:[0,1]
	v_pk_mul_f32 v[104:105], v[192:193], v[104:105] op_sel_hi:[0,1]
	v_pk_mul_f32 v[102:103], v[192:193], v[102:103] op_sel_hi:[0,1]
	v_pk_mul_f32 v[100:101], v[192:193], v[100:101] op_sel_hi:[0,1]
	v_pk_mul_f32 v[98:99], v[192:193], v[98:99] op_sel_hi:[0,1]
	v_pk_mul_f32 v[96:97], v[192:193], v[96:97] op_sel_hi:[0,1]
	s_waitcnt lgkmcnt(0)
	v_mov_b32_e32 v192, v197
	v_pk_mul_f32 v[78:79], v[78:79], v[192:193] op_sel_hi:[1,0]
	v_pk_mul_f32 v[76:77], v[76:77], v[192:193] op_sel_hi:[1,0]
	v_pk_mul_f32 v[74:75], v[74:75], v[192:193] op_sel_hi:[1,0]
	v_pk_mul_f32 v[72:73], v[72:73], v[192:193] op_sel_hi:[1,0]
	v_pk_mul_f32 v[70:71], v[70:71], v[192:193] op_sel_hi:[1,0]
	v_pk_mul_f32 v[68:69], v[68:69], v[192:193] op_sel_hi:[1,0]
	v_pk_mul_f32 v[66:67], v[66:67], v[192:193] op_sel_hi:[1,0]
	v_pk_mul_f32 v[64:65], v[64:65], v[192:193] op_sel_hi:[1,0]
	s_barrier
; #define LAS __attribute__((address_space(3)))
; #define MFMA32(a, b, c) __builtin_amdgcn_mfma_f32_32x32x16_bf16((a), (b), (c), 0, 0, 0)
; template <bool PASS2, int DIRT>
; DI void mlstm_item(const Params& P, LAS unsigned char* lds, int st, int g) {
;     ...
;             {
;                 bf16x8 pf[2][4];
;                 auto ldp = [&](int ks, bf16x8 (&pb)[4]) {
; #pragma unroll
;                     for (int jt = 0; jt < 4; ++jt) { const bool on = dir ? (ks >= 2 * jt) : (ks <= 2 * jt + 1); if (on) pb[jt] = *(const LAS bf16x8*)(PS + off_b(32 * jt + r, 2 * ks + hh)); } };
;                 ldp(0, pf[0]);
; #pragma unroll
;                 for (int ks = 0; ks < 8; ++ks) {
;                     if (ks + 1 < 8) ldp(ks + 1, pf[(ks + 1) & 1]);
;                     __builtin_amdgcn_sched_barrier(0);
; #pragma unroll
;                     for (int jt = 0; jt < 4; ++jt) { const bool on = dir ? (ks >= 2 * jt) : (ks <= 2 * jt + 1); if (on) num[jt] = MFMA32(vf[ks], pf[ks & 1][jt], num[jt]); }
;                     __builtin_amdgcn_sched_barrier(0); }
;                 asm volatile("" : "+v"(num[0]), "+v"(num[1]), "+v"(num[2]), "+v"(num[3]) :: "memory");
;             }
;             bf16_t* Hd = (bf16_t*)(P.ws + (dir ? WS_HB : WS_HF));
; #pragma unroll
;             for (int jt = 0; jt < 4; ++jt) { const int j = 32 * jt + r;
;                 const float den = (sDENP[j] + sDENP[128 + j]) + (sDENP[256 + j] + sDENP[384 + j]) + sWST[j] * ((sQNP[j] + sQNP[128 + j]) + (sQNP[256 + j] + sQNP[384 + j]));
;                 const float inv = 1.0f / fmaxf(fabsf(den), sCL[j]);
	v_mbcnt_lo_u32_b32 v192, -1, 0
	v_mbcnt_hi_u32_b32 v192, -1, v192
	v_pk_mul_f32 v[94:95], v[94:95], v[196:197] op_sel_hi:[1,0]
	v_or_b32_e32 v192, s97, v192
	v_pk_mul_f32 v[92:93], v[92:93], v[196:197] op_sel_hi:[1,0]
	v_and_b32_e32 v195, 31, v192
	v_bfe_u32 v192, v192, 5, 1
	v_pk_mul_f32 v[90:91], v[90:91], v[196:197] op_sel_hi:[1,0]
	v_pk_mul_f32 v[88:89], v[88:89], v[196:197] op_sel_hi:[1,0]
	v_pk_mul_f32 v[86:87], v[86:87], v[196:197] op_sel_hi:[1,0]
	v_pk_mul_f32 v[84:85], v[84:85], v[196:197] op_sel_hi:[1,0]
	v_pk_mul_f32 v[82:83], v[82:83], v[196:197] op_sel_hi:[1,0]
	v_pk_mul_f32 v[80:81], v[80:81], v[196:197] op_sel_hi:[1,0]
	v_mul_u32_u24_e32 v196, 0x110, v195
	v_lshlrev_b32_e32 v197, 4, v192
	v_add3_u32 v196, s3, v197, v196
	ds_read_b128 v[206:209], v196 offset:8704
	ds_read_b128 v[210:213], v196 offset:17408
	ds_read_b128 v[214:217], v196 offset:26112
	ds_read_b128 v[218:221], v196
	ds_read_b128 v[222:225], v196 offset:32
	ds_read_b128 v[226:229], v196 offset:8736
	ds_read_b128 v[230:233], v196 offset:17440
	ds_read_b128 v[234:237], v196 offset:26144
	s_waitcnt vmcnt(7) lgkmcnt(7)
	v_mfma_f32_32x32x16_bf16 v[96:111], v[188:191], v[206:209], v[96:111]
	s_waitcnt lgkmcnt(6)
	v_mfma_f32_32x32x16_bf16 v[80:95], v[188:191], v[210:213], v[80:95]
	s_waitcnt lgkmcnt(5)
	v_mfma_f32_32x32x16_bf16 v[64:79], v[188:191], v[214:217], v[64:79]
	s_waitcnt lgkmcnt(4)
	v_mfma_f32_32x32x16_bf16 v[112:127], v[188:191], v[218:221], v[112:127]
	ds_read_b128 v[206:209], v196 offset:8768
	ds_read_b128 v[210:213], v196 offset:17472
	ds_read_b128 v[214:217], v196 offset:26176
	s_waitcnt vmcnt(6) lgkmcnt(5)
	v_mfma_f32_32x32x16_bf16 v[96:111], v[184:187], v[226:229], v[96:111]
	s_waitcnt lgkmcnt(4)
	v_mfma_f32_32x32x16_bf16 v[80:95], v[184:187], v[230:233], v[80:95]
	s_waitcnt lgkmcnt(3)
	v_mfma_f32_32x32x16_bf16 v[64:79], v[184:187], v[234:237], v[64:79]
	v_mfma_f32_32x32x16_bf16 v[112:127], v[184:187], v[222:225], v[112:127]
	ds_read_b128 v[218:221], v196 offset:8800
	ds_read_b128 v[222:225], v196 offset:17504
	ds_read_b128 v[226:229], v196 offset:26208
	s_waitcnt vmcnt(5) lgkmcnt(5)
	v_mfma_f32_32x32x16_bf16 v[96:111], v[180:183], v[206:209], v[96:111]
	s_waitcnt lgkmcnt(4)
	v_mfma_f32_32x32x16_bf16 v[80:95], v[180:183], v[210:213], v[80:95]
	s_waitcnt lgkmcnt(3)
	v_mfma_f32_32x32x16_bf16 v[64:79], v[180:183], v[214:217], v[64:79]
	ds_read_b128 v[206:209], v196 offset:17536
	ds_read_b128 v[210:213], v196 offset:26240
	s_waitcnt vmcnt(4) lgkmcnt(4)
	v_mfma_f32_32x32x16_bf16 v[96:111], v[176:179], v[218:221], v[96:111]
	s_waitcnt lgkmcnt(3)
	v_mfma_f32_32x32x16_bf16 v[80:95], v[176:179], v[222:225], v[80:95]
	s_waitcnt lgkmcnt(2)
	v_mfma_f32_32x32x16_bf16 v[64:79], v[176:179], v[226:229], v[64:79]
	ds_read_b128 v[214:217], v196 offset:17568
	ds_read_b128 v[218:221], v196 offset:26272
	s_waitcnt vmcnt(3) lgkmcnt(3)
	v_mfma_f32_32x32x16_bf16 v[80:95], v[172:175], v[206:209], v[80:95]
	s_waitcnt lgkmcnt(2)
	v_mfma_f32_32x32x16_bf16 v[64:79], v[172:175], v[210:213], v[64:79]
	ds_read_b128 v[206:209], v196 offset:26304
	s_waitcnt vmcnt(2) lgkmcnt(2)
	v_mfma_f32_32x32x16_bf16 v[80:95], v[168:171], v[214:217], v[80:95]
	s_waitcnt lgkmcnt(1)
	v_mfma_f32_32x32x16_bf16 v[64:79], v[168:171], v[218:221], v[64:79]
	ds_read_b128 v[210:213], v196 offset:26336
	s_waitcnt vmcnt(1) lgkmcnt(1)
	v_mfma_f32_32x32x16_bf16 v[64:79], v[164:167], v[206:209], v[64:79]
	s_waitcnt vmcnt(0) lgkmcnt(0)
	v_mfma_f32_32x32x16_bf16 v[64:79], v[160:163], v[210:213], v[64:79]
	v_lshlrev_b32_e32 v192, 3, v192
	s_add_i32 s3, 0, 0x1a800
	v_lshlrev_b32_e32 v206, 2, v195
	v_lshl_add_u64 v[196:197], s[14:15], 0, v[192:193]
	v_add_u32_e32 v192, s3, v206
	ds_read_b32 v208, v192
	v_or_b32_e32 v192, 0x200, v206
	v_add_u32_e32 v207, s3, v192
	v_add_u32_e32 v192, s95, v192
	ds_read_b32 v210, v207
	ds_read_b32 v211, v192
	v_or_b32_e32 v207, 0x400, v206
	v_add_u32_e32 v209, s3, v207
	v_or_b32_e32 v215, 0x600, v206
	v_add_u32_e32 v192, s95, v207
	ds_read_b32 v212, v209
	ds_read_b32 v213, v192
	v_add_u32_e32 v209, s3, v215
	v_add_u32_e32 v192, s95, v215
	s_add_i32 s4, 0, 0x19e00
	ds_read_b32 v214, v209
	ds_read_b32 v215, v192
	v_add_u32_e32 v209, s2, v206
	v_add_u32_e32 v192, s4, v206
	ds_read_b32 v216, v209
	ds_read_b32 v192, v192
	v_add_u32_e32 v209, s95, v206
	ds_read_b32 v209, v209
	s_waitcnt lgkmcnt(1)
	v_max_f32_e32 v192, v192, v192
	s_waitcnt lgkmcnt(0)
; DI unsigned pk2(float a, float b) { f32x2 f = {a, b}; bf16x2_t h = __builtin_convertvector(f, bf16x2_t); return __builtin_bit_cast(unsigned, h); }
; template <bool PASS2, int DIRT>
; DI void mlstm_item(const Params& P, LAS unsigned char* lds, int st, int g) {
;     ...
;             for (int jt = 0; jt < 4; ++jt) { const int j = 32 * jt + r;
;                 const float den = (sDENP[j] + sDENP[128 + j]) + (sDENP[256 + j] + sDENP[384 + j]) + sWST[j] * ((sQNP[j] + sQNP[128 + j]) + (sQNP[256 + j] + sQNP[384 + j]));
;                 const float inv = 1.0f / fmaxf(fabsf(den), sCL[j]);
;                 bf16_t* hp = Hd + (size_t)(tok0 + j) * 1024 + h * 256 + 32 * wid + 4 * hh;
; #pragma unroll
;                 for (int gq = 0; gq < 4; ++gq) { u32x2 w; w.x = pk2(num[jt][4 * gq] * inv, num[jt][4 * gq + 1] * inv); w.y = pk2(num[jt][4 * gq + 2] * inv, num[jt][4 * gq + 3] * inv); *(u32x2*)(hp + 8 * gq) = w; } }
	v_pk_add_f32 v[208:209], v[208:209], v[210:211]
	v_pk_add_f32 v[210:211], v[212:213], v[214:215]
	s_nop 0
	v_pk_add_f32 v[208:209], v[208:209], v[210:211]
	s_nop 0
	v_fmac_f32_e32 v208, v216, v209
	v_max_f32_e64 v192, |v208|, v192
	v_div_scale_f32 v207, s[44:45], v192, v192, 1.0
	v_rcp_f32_e32 v208, v207
	s_nop 0
	v_fma_f32 v209, -v207, v208, 1.0
	v_fmac_f32_e32 v208, v209, v208
	v_div_scale_f32 v209, vcc, 1.0, v192, 1.0
	v_mul_f32_e32 v210, v209, v208
	v_fma_f32 v211, -v207, v210, v209
	v_fmac_f32_e32 v210, v211, v208
	v_fma_f32 v207, -v207, v210, v209
	v_div_fmas_f32 v207, v207, v208, v210
	v_div_fixup_f32 v208, v207, v192, 1.0
	v_or_b32_e32 v192, s67, v195
	v_lshlrev_b32_e32 v192, 11, v192
	v_pk_mul_f32 v[112:113], v[112:113], v[208:209] op_sel_hi:[1,0]
	v_pk_mul_f32 v[114:115], v[114:115], v[208:209] op_sel_hi:[1,0]
	v_lshl_add_u64 v[210:211], v[196:197], 0, v[192:193]
	v_cvt_pk_bf16_f32 v244, v112, v113
	v_cvt_pk_bf16_f32 v245, v114, v115
	v_pk_mul_f32 v[112:113], v[116:117], v[208:209] op_sel_hi:[1,0]
	v_pk_mul_f32 v[114:115], v[118:119], v[208:209] op_sel_hi:[1,0]
	v_cvt_pk_bf16_f32 v248, v112, v113
	v_cvt_pk_bf16_f32 v249, v114, v115
	v_pk_mul_f32 v[112:113], v[120:121], v[208:209] op_sel_hi:[1,0]
	v_pk_mul_f32 v[114:115], v[122:123], v[208:209] op_sel_hi:[1,0]
	v_cvt_pk_bf16_f32 v246, v112, v113
	v_cvt_pk_bf16_f32 v247, v114, v115
	v_pk_mul_f32 v[112:113], v[124:125], v[208:209] op_sel_hi:[1,0]
	v_pk_mul_f32 v[114:115], v[126:127], v[208:209] op_sel_hi:[1,0]
	v_or_b32_e32 v120, 32, v195
	v_cvt_pk_bf16_f32 v250, v112, v113
	v_cvt_pk_bf16_f32 v251, v114, v115
	v_lshlrev_b32_e32 v121, 2, v120
	v_or_b32_e32 v115, 0x280, v206
	v_mbcnt_lo_u32_b32 v252, -1, 0
	v_mbcnt_hi_u32_b32 v252, -1, v252
	v_lshrrev_b32_e32 v252, 5, v252
	v_mul_u32_u24_e32 v252, 24, v252
	v_mov_b32_e32 v253, 0
	v_permlane32_swap_b32_e32 v244, v246
	v_permlane32_swap_b32_e32 v245, v247
	v_permlane32_swap_b32_e32 v248, v250
	v_permlane32_swap_b32_e32 v249, v251
	v_lshl_add_u64 v[252:253], v[210:211], 0, v[252:253]
	global_store_dwordx4 v[252:253], v[244:247], off
	global_store_dwordx4 v[252:253], v[248:251], off offset:16
	v_add_u32_e32 v112, s3, v121
	v_add_u32_e32 v113, s3, v115
	v_or_b32_e32 v117, 0x480, v206
	v_add_u32_e32 v115, s95, v115
	ds_read_b32 v112, v112
	ds_read_b32 v114, v113
	ds_read_b32 v115, v115
	v_add_u32_e32 v113, s3, v117
	v_or_b32_e32 v119, 0x680, v206
	v_add_u32_e32 v117, s95, v117
	ds_read_b32 v116, v113
	ds_read_b32 v117, v117
	v_add_u32_e32 v113, s3, v119
	v_add_u32_e32 v119, s95, v119
	ds_read_b32 v118, v113
	ds_read_b32 v119, v119
	v_add_u32_e32 v113, s2, v121
	ds_read_b32 v122, v113
	v_add_u32_e32 v113, s95, v121
	ds_read_b32 v113, v113
	s_waitcnt lgkmcnt(0)
	v_pk_add_f32 v[112:113], v[112:113], v[114:115]
	v_pk_add_f32 v[114:115], v[116:117], v[118:119]
	s_nop 0
	v_pk_add_f32 v[112:113], v[112:113], v[114:115]
	s_nop 0
	v_fmac_f32_e32 v112, v122, v113
	v_add_u32_e32 v113, s4, v121
	ds_read_b32 v113, v113
	s_waitcnt lgkmcnt(0)
	v_max_f32_e32 v113, v113, v113
	v_max_f32_e64 v112, |v112|, v113
	v_div_scale_f32 v113, s[44:45], v112, v112, 1.0
	v_rcp_f32_e32 v114, v113
	s_nop 0
	v_fma_f32 v115, -v113, v114, 1.0
	v_fmac_f32_e32 v114, v115, v114
	v_div_scale_f32 v115, vcc, 1.0, v112, 1.0
	v_mul_f32_e32 v116, v115, v114
	v_fma_f32 v117, -v113, v116, v115
	v_fmac_f32_e32 v116, v117, v114
	v_fma_f32 v113, -v113, v116, v115
	v_div_fmas_f32 v113, v113, v114, v116
	v_div_fixup_f32 v112, v113, v112, 1.0
	v_or_b32_e32 v113, s67, v120
	v_lshlrev_b32_e32 v192, 11, v113
	v_pk_mul_f32 v[96:97], v[96:97], v[112:113] op_sel_hi:[1,0]
	v_pk_mul_f32 v[98:99], v[98:99], v[112:113] op_sel_hi:[1,0]
	v_lshl_add_u64 v[114:115], v[196:197], 0, v[192:193]
	v_cvt_pk_bf16_f32 v244, v96, v97
	v_cvt_pk_bf16_f32 v245, v98, v99
	v_pk_mul_f32 v[96:97], v[100:101], v[112:113] op_sel_hi:[1,0]
	v_pk_mul_f32 v[98:99], v[102:103], v[112:113] op_sel_hi:[1,0]
	v_cvt_pk_bf16_f32 v248, v96, v97
	v_cvt_pk_bf16_f32 v249, v98, v99
	v_pk_mul_f32 v[96:97], v[104:105], v[112:113] op_sel_hi:[1,0]
	v_pk_mul_f32 v[98:99], v[106:107], v[112:113] op_sel_hi:[1,0]
	v_cvt_pk_bf16_f32 v246, v96, v97
	v_cvt_pk_bf16_f32 v247, v98, v99
	v_pk_mul_f32 v[96:97], v[108:109], v[112:113] op_sel_hi:[1,0]
	v_pk_mul_f32 v[98:99], v[110:111], v[112:113] op_sel_hi:[1,0]
	v_or_b32_e32 v104, 64, v195
	v_cvt_pk_bf16_f32 v250, v96, v97
	v_cvt_pk_bf16_f32 v251, v98, v99
	v_lshlrev_b32_e32 v105, 2, v104
	v_or_b32_e32 v99, 0x300, v206
	v_mbcnt_lo_u32_b32 v252, -1, 0
	v_mbcnt_hi_u32_b32 v252, -1, v252
	v_lshrrev_b32_e32 v252, 5, v252
	v_mul_u32_u24_e32 v252, 24, v252
	v_mov_b32_e32 v253, 0
	v_permlane32_swap_b32_e32 v244, v246
	v_permlane32_swap_b32_e32 v245, v247
	v_permlane32_swap_b32_e32 v248, v250
	v_permlane32_swap_b32_e32 v249, v251
	v_lshl_add_u64 v[252:253], v[114:115], 0, v[252:253]
	global_store_dwordx4 v[252:253], v[244:247], off
	global_store_dwordx4 v[252:253], v[248:251], off offset:16
	v_add_u32_e32 v96, s3, v105
	v_add_u32_e32 v97, s3, v99
	v_or_b32_e32 v101, 0x500, v206
	v_add_u32_e32 v99, s95, v99
	ds_read_b32 v96, v96
	ds_read_b32 v98, v97
	ds_read_b32 v99, v99
	v_add_u32_e32 v97, s3, v101
	v_or_b32_e32 v103, 0x700, v206
	v_add_u32_e32 v101, s95, v101
	ds_read_b32 v100, v97
	ds_read_b32 v101, v101
	v_add_u32_e32 v97, s3, v103
	v_add_u32_e32 v103, s95, v103
	ds_read_b32 v102, v97
	ds_read_b32 v103, v103
	v_add_u32_e32 v97, s2, v105
	ds_read_b32 v106, v97
	v_add_u32_e32 v97, s95, v105
	ds_read_b32 v97, v97
	s_waitcnt lgkmcnt(0)
	v_pk_add_f32 v[96:97], v[96:97], v[98:99]
	v_pk_add_f32 v[98:99], v[100:101], v[102:103]
	s_nop 0
	v_pk_add_f32 v[96:97], v[96:97], v[98:99]
	s_nop 0
	v_fmac_f32_e32 v96, v106, v97
	v_add_u32_e32 v97, s4, v105
	ds_read_b32 v97, v97
	s_waitcnt lgkmcnt(0)
; DI int lane_id() { int l; asm volatile("v_mbcnt_lo_u32_b32 %0, -1, 0\n\tv_mbcnt_hi_u32_b32 %0, -1, %0" : "=v"(l)); return l; }
; DI unsigned pk2(float a, float b) { f32x2 f = {a, b}; bf16x2_t h = __builtin_convertvector(f, bf16x2_t); return __builtin_bit_cast(unsigned, h); }
; template <bool PASS2, int DIRT>
; DI void mlstm_item(const Params& P, LAS unsigned char* lds, int st, int g) {
;     ...
;             for (int jt = 0; jt < 4; ++jt) { const int j = 32 * jt + r;
;                 const float den = (sDENP[j] + sDENP[128 + j]) + (sDENP[256 + j] + sDENP[384 + j]) + sWST[j] * ((sQNP[j] + sQNP[128 + j]) + (sQNP[256 + j] + sQNP[384 + j]));
;                 const float inv = 1.0f / fmaxf(fabsf(den), sCL[j]);
;                 bf16_t* hp = Hd + (size_t)(tok0 + j) * 1024 + h * 256 + 32 * wid + 4 * hh;
; #pragma unroll
;                 for (int gq = 0; gq < 4; ++gq) { u32x2 w; w.x = pk2(num[jt][4 * gq] * inv, num[jt][4 * gq + 1] * inv); w.y = pk2(num[jt][4 * gq + 2] * inv, num[jt][4 * gq + 3] * inv); *(u32x2*)(hp + 8 * gq) = w; } }
;         }
;         tid = (wid << 6) | lane_id(); asm volatile("" : "+v"(tid)); lane = tid & 63; r = lane & 31; hh = lane >> 5;
;         if (ci + 1 < nchunks) { const int tokn = chunk_tok0(ci + 1);
; #pragma unroll
;             for (int i = 0; i < 4; ++i) { const int n = tid + 512 * i, row = n >> 4, ch = n & 15; kq[i] = *(const u32x4*)(Kg + (size_t)(tokn + row) * 512 + h * 128 + ch * 8);
;                 if (PASS2) kq[4 + i] = *(const u32x4*)(Qg + (size_t)(tokn + row) * 512 + h * 128 + ch * 8); } }
	v_max_f32_e32 v97, v97, v97
	v_max_f32_e64 v96, |v96|, v97
	v_div_scale_f32 v97, s[44:45], v96, v96, 1.0
	v_rcp_f32_e32 v98, v97
	s_nop 0
	v_fma_f32 v99, -v97, v98, 1.0
	v_fmac_f32_e32 v98, v99, v98
	v_div_scale_f32 v99, vcc, 1.0, v96, 1.0
	v_mul_f32_e32 v100, v99, v98
	v_fma_f32 v101, -v97, v100, v99
	v_fmac_f32_e32 v100, v101, v98
	v_fma_f32 v97, -v97, v100, v99
	v_div_fmas_f32 v97, v97, v98, v100
	v_div_fixup_f32 v96, v97, v96, 1.0
	v_or_b32_e32 v97, s67, v104
	v_lshlrev_b32_e32 v192, 11, v97
	v_pk_mul_f32 v[80:81], v[80:81], v[96:97] op_sel_hi:[1,0]
	v_pk_mul_f32 v[82:83], v[82:83], v[96:97] op_sel_hi:[1,0]
	v_lshl_add_u64 v[98:99], v[196:197], 0, v[192:193]
	v_cvt_pk_bf16_f32 v244, v80, v81
	v_cvt_pk_bf16_f32 v245, v82, v83
	v_pk_mul_f32 v[80:81], v[84:85], v[96:97] op_sel_hi:[1,0]
	v_pk_mul_f32 v[82:83], v[86:87], v[96:97] op_sel_hi:[1,0]
	v_cvt_pk_bf16_f32 v248, v80, v81
	v_cvt_pk_bf16_f32 v249, v82, v83
	v_pk_mul_f32 v[80:81], v[88:89], v[96:97] op_sel_hi:[1,0]
	v_pk_mul_f32 v[82:83], v[90:91], v[96:97] op_sel_hi:[1,0]
	v_cvt_pk_bf16_f32 v246, v80, v81
	v_cvt_pk_bf16_f32 v247, v82, v83
	v_pk_mul_f32 v[80:81], v[92:93], v[96:97] op_sel_hi:[1,0]
	v_pk_mul_f32 v[82:83], v[94:95], v[96:97] op_sel_hi:[1,0]
	v_or_b32_e32 v88, 0x60, v195
	v_cvt_pk_bf16_f32 v250, v80, v81
	v_cvt_pk_bf16_f32 v251, v82, v83
	v_lshlrev_b32_e32 v89, 2, v88
	v_or_b32_e32 v83, 0x380, v206
	v_mbcnt_lo_u32_b32 v252, -1, 0
	v_mbcnt_hi_u32_b32 v252, -1, v252
	v_lshrrev_b32_e32 v252, 5, v252
	v_mul_u32_u24_e32 v252, 24, v252
	v_mov_b32_e32 v253, 0
	v_permlane32_swap_b32_e32 v244, v246
	v_permlane32_swap_b32_e32 v245, v247
	v_permlane32_swap_b32_e32 v248, v250
	v_permlane32_swap_b32_e32 v249, v251
	v_lshl_add_u64 v[252:253], v[98:99], 0, v[252:253]
	global_store_dwordx4 v[252:253], v[244:247], off
	global_store_dwordx4 v[252:253], v[248:251], off offset:16
	v_add_u32_e32 v80, s3, v89
	v_add_u32_e32 v81, s3, v83
	v_or_b32_e32 v85, 0x580, v206
	v_add_u32_e32 v83, s95, v83
	ds_read_b32 v80, v80
	ds_read_b32 v82, v81
	ds_read_b32 v83, v83
	v_add_u32_e32 v81, s3, v85
	v_or_b32_e32 v87, 0x780, v206
	v_add_u32_e32 v85, s95, v85
	ds_read_b32 v84, v81
	ds_read_b32 v85, v85
	v_add_u32_e32 v81, s3, v87
	v_add_u32_e32 v87, s95, v87
	ds_read_b32 v86, v81
	ds_read_b32 v87, v87
	v_add_u32_e32 v81, s2, v89
	ds_read_b32 v90, v81
	v_add_u32_e32 v81, s95, v89
	ds_read_b32 v81, v81
	s_waitcnt lgkmcnt(0)
	v_pk_add_f32 v[80:81], v[80:81], v[82:83]
	v_pk_add_f32 v[82:83], v[84:85], v[86:87]
	s_nop 0
	v_pk_add_f32 v[80:81], v[80:81], v[82:83]
	s_nop 0
	v_fmac_f32_e32 v80, v90, v81
	v_add_u32_e32 v81, s4, v89
	ds_read_b32 v81, v81
	s_add_i32 s4, s72, 1
	s_cmp_lg_u32 s72, 7
	s_waitcnt lgkmcnt(0)
	v_max_f32_e32 v81, v81, v81
	v_max_f32_e64 v80, |v80|, v81
	v_div_scale_f32 v81, s[2:3], v80, v80, 1.0
	v_rcp_f32_e32 v82, v81
	s_mov_b64 s[2:3], -1
	v_fma_f32 v83, -v81, v82, 1.0
	v_fmac_f32_e32 v82, v83, v82
	v_div_scale_f32 v83, vcc, 1.0, v80, 1.0
	v_mul_f32_e32 v84, v83, v82
	v_fma_f32 v85, -v81, v84, v83
	v_fmac_f32_e32 v84, v85, v82
	v_fma_f32 v81, -v81, v84, v83
	v_div_fmas_f32 v81, v81, v82, v84
	v_div_fixup_f32 v80, v81, v80, 1.0
	v_or_b32_e32 v81, s67, v88
	v_lshlrev_b32_e32 v192, 11, v81
	v_pk_mul_f32 v[64:65], v[64:65], v[80:81] op_sel_hi:[1,0]
	v_pk_mul_f32 v[66:67], v[66:67], v[80:81] op_sel_hi:[1,0]
	v_lshl_add_u64 v[82:83], v[196:197], 0, v[192:193]
	v_cvt_pk_bf16_f32 v244, v64, v65
	v_cvt_pk_bf16_f32 v245, v66, v67
	v_pk_mul_f32 v[64:65], v[68:69], v[80:81] op_sel_hi:[1,0]
	v_pk_mul_f32 v[66:67], v[70:71], v[80:81] op_sel_hi:[1,0]
	v_cvt_pk_bf16_f32 v248, v64, v65
	v_cvt_pk_bf16_f32 v249, v66, v67
	v_pk_mul_f32 v[64:65], v[72:73], v[80:81] op_sel_hi:[1,0]
	v_pk_mul_f32 v[66:67], v[74:75], v[80:81] op_sel_hi:[1,0]
	v_cvt_pk_bf16_f32 v246, v64, v65
	v_cvt_pk_bf16_f32 v247, v66, v67
	v_pk_mul_f32 v[64:65], v[76:77], v[80:81] op_sel_hi:[1,0]
	v_pk_mul_f32 v[66:67], v[78:79], v[80:81] op_sel_hi:[1,0]
	v_cvt_pk_bf16_f32 v250, v64, v65
	v_cvt_pk_bf16_f32 v251, v66, v67
	v_mbcnt_lo_u32_b32 v252, -1, 0
	v_mbcnt_hi_u32_b32 v252, -1, v252
	v_lshrrev_b32_e32 v252, 5, v252
	v_mul_u32_u24_e32 v252, 24, v252
	v_mov_b32_e32 v253, 0
	v_permlane32_swap_b32_e32 v244, v246
	v_permlane32_swap_b32_e32 v245, v247
	v_permlane32_swap_b32_e32 v248, v250
	v_permlane32_swap_b32_e32 v249, v251
	v_lshl_add_u64 v[252:253], v[82:83], 0, v[252:253]
	global_store_dwordx4 v[252:253], v[244:247], off
	global_store_dwordx4 v[252:253], v[248:251], off offset:16
	v_mbcnt_lo_u32_b32 v64, -1, 0
	v_mbcnt_hi_u32_b32 v64, -1, v64
	s_nop 0
	v_or_b32_e32 v97, s97, v64
	s_nop 0
	v_lshlrev_b32_e32 v96, 3, v97
	s_cbranch_scc0 .LBB0_812
	s_lshl_b32 s2, s4, 7
	v_lshlrev_b32_e32 v64, 4, v97
	v_add_u32_e32 v72, 0x200, v97
	v_add_u32_e32 v80, 0x400, v97
	v_add_u32_e32 v92, 0x600, v97
	s_add_i32 s2, s2, s43
	v_and_b32_e32 v192, 0xf0, v64
	v_ashrrev_i32_e32 v64, 4, v97
	v_ashrrev_i32_e32 v72, 4, v72
	v_ashrrev_i32_e32 v80, 4, v80
	v_ashrrev_i32_e32 v92, 4, v92
	v_add_u32_e32 v64, s2, v64
	v_add_u32_e32 v72, s2, v72
	v_add_u32_e32 v80, s2, v80
	v_add_u32_e32 v92, s2, v92
	v_ashrrev_i32_e32 v65, 31, v64
	v_ashrrev_i32_e32 v73, 31, v72
	v_ashrrev_i32_e32 v81, 31, v80
	v_ashrrev_i32_e32 v93, 31, v92
	v_lshl_add_u64 v[88:89], s[6:7], 0, v[192:193]
	v_lshl_add_u64 v[90:91], s[8:9], 0, v[192:193]
	v_lshlrev_b64 v[64:65], 10, v[64:65]
	v_lshlrev_b64 v[72:73], 10, v[72:73]
	v_lshlrev_b64 v[80:81], 10, v[80:81]
	v_lshlrev_b64 v[92:93], 10, v[92:93]
	v_lshl_add_u64 v[66:67], v[88:89], 0, v[64:65]
	v_lshl_add_u64 v[64:65], v[90:91], 0, v[64:65]
	v_lshl_add_u64 v[74:75], v[88:89], 0, v[72:73]
	v_lshl_add_u64 v[72:73], v[90:91], 0, v[72:73]
	v_lshl_add_u64 v[82:83], v[88:89], 0, v[80:81]
	v_lshl_add_u64 v[80:81], v[90:91], 0, v[80:81]
	v_lshl_add_u64 v[88:89], v[88:89], 0, v[92:93]
	v_lshl_add_u64 v[90:91], v[90:91], 0, v[92:93]
	global_load_dwordx4 v[68:71], v[66:67], off
	s_nop 0
	global_load_dwordx4 v[64:67], v[64:65], off
	s_nop 0
	global_load_dwordx4 v[76:79], v[74:75], off
	s_nop 0
	global_load_dwordx4 v[72:75], v[72:73], off
	s_nop 0
	global_load_dwordx4 v[84:87], v[82:83], off
	s_nop 0
	global_load_dwordx4 v[80:83], v[80:81], off
	s_nop 0
	global_load_dwordx4 v[92:95], v[88:89], off
	s_nop 0
	global_load_dwordx4 v[88:91], v[90:91], off
	v_lshlrev_b32_e32 v98, 3, v97
	s_mov_b64 s[2:3], 0
